# v18 plus the eight K-loop back-edge targets aligned to 64 bytes (s_nop padding, executed once per unit)
# baseline (speedup 1.0000x reference)
.LBB0_260:
	s_ashr_i32 s41, s40, 31
	s_lshl_b64 s[42:43], s[40:41], 19
	s_add_u32 s42, s54, s42
	s_addc_u32 s43, s55, s43
	s_and_b64 s[44:45], s[4:5], exec
	ds_read_b128 v[0:3], v219
	ds_read_b128 v[4:7], v219 offset:1024
	ds_read_b128 v[8:11], v219 offset:2048
	s_waitcnt vmcnt(2)
	ds_read_b128 v[12:15], v219 offset:3072
	s_waitcnt vmcnt(1)
	ds_read_b128 v[16:19], v220
	s_waitcnt vmcnt(0)
	ds_read_b128 v[20:23], v220 offset:1024
	ds_read_b128 v[24:27], v220 offset:2048
	ds_read_b128 v[28:31], v220 offset:3072
	s_cselect_b32 s7, s43, s13
	s_cselect_b32 s11, s42, s12
	s_ashr_i32 s39, s38, 31
	s_lshl_b64 s[44:45], s[38:39], 19
	s_add_u32 s44, s56, s44
	s_addc_u32 s45, s57, s45
	s_and_b64 s[46:47], s[4:5], exec
	s_cselect_b32 s39, s45, s9
	s_cselect_b32 s41, s44, s8
	s_add_u32 s46, s12, 0x100
	s_addc_u32 s47, s13, 0
	s_add_u32 s52, s8, 0x100
	s_addc_u32 s53, s9, 0
	s_add_u32 s48, s12, 0x180
	s_addc_u32 s49, s13, 0
	ds_read_b128 v[32:35], v221
	ds_read_b128 v[36:39], v221 offset:1024
	ds_read_b128 v[40:43], v221 offset:2048
	ds_read_b128 v[44:47], v221 offset:3072
	ds_read_b128 v[48:51], v221 offset:4096
	ds_read_b128 v[52:55], v221 offset:5120
	ds_read_b128 v[56:59], v221 offset:6144
	ds_read_b128 v[60:63], v221 offset:7168
	s_add_u32 s50, s8, 0x180
	s_addc_u32 s51, s9, 0
	s_add_u32 s76, s12, 0x40080
	s_addc_u32 s77, s13, 0
	s_add_i32 m0, s59, 0xc000
	s_nop 0
	global_load_lds_dwordx4 v215, s[76:77]
	s_nop 0
	s_add_i32 m0, s59, 0xe000
	s_nop 0
	global_load_lds_dwordx4 v217, s[76:77]
	s_waitcnt vmcnt(8) lgkmcnt(0)
	s_barrier
	s_waitcnt lgkmcnt(7)
	v_mfma_i32_16x16x64_i8 v[64:67], v[0:3], v[32:35], 0
	s_mov_b32 s76, 0
	v_mfma_i32_16x16x64_i8 v[68:71], v[8:11], v[32:35], 0
	s_waitcnt lgkmcnt(5)
	v_mfma_i32_16x16x64_i8 v[72:75], v[0:3], v[40:43], 0
	v_mfma_i32_16x16x64_i8 v[76:79], v[8:11], v[40:43], 0
	s_waitcnt lgkmcnt(3)
	v_mfma_i32_16x16x64_i8 v[84:87], v[8:11], v[48:51], 0
	s_waitcnt lgkmcnt(1)
	v_mfma_i32_16x16x64_i8 v[88:91], v[0:3], v[56:59], 0
	v_mfma_i32_16x16x64_i8 v[140:143], v[4:7], v[36:39], v[64:67]
	v_mfma_i32_16x16x64_i8 v[144:147], v[12:15], v[36:39], v[68:71]
	v_mfma_i32_16x16x64_i8 v[152:155], v[4:7], v[44:47], v[72:75]
	v_mfma_i32_16x16x64_i8 v[156:159], v[12:15], v[44:47], v[76:79]
	v_mfma_i32_16x16x64_i8 v[80:83], v[0:3], v[48:51], 0
	v_mfma_i32_16x16x64_i8 v[84:87], v[12:15], v[52:55], v[84:87]
	s_waitcnt lgkmcnt(0)
	v_mfma_i32_16x16x64_i8 v[88:91], v[4:7], v[60:63], v[88:91]
	v_mfma_i32_16x16x64_i8 v[92:95], v[8:11], v[56:59], 0
	v_mfma_i32_16x16x64_i8 v[80:83], v[4:7], v[52:55], v[80:83]
	v_mfma_i32_16x16x64_i8 v[92:95], v[12:15], v[60:63], v[92:95]
	v_mfma_i32_16x16x64_i8 v[96:99], v[16:19], v[32:35], 0
	v_mfma_i32_16x16x64_i8 v[32:35], v[24:27], v[32:35], 0
	v_mfma_i32_16x16x64_i8 v[96:99], v[20:23], v[36:39], v[96:99]
	v_mfma_i32_16x16x64_i8 v[32:35], v[28:31], v[36:39], v[32:35]
	v_mfma_i32_16x16x64_i8 v[36:39], v[16:19], v[40:43], 0
	v_mfma_i32_16x16x64_i8 v[40:43], v[24:27], v[40:43], 0
	v_mfma_i32_16x16x64_i8 v[36:39], v[20:23], v[44:47], v[36:39]
	v_mfma_i32_16x16x64_i8 v[40:43], v[28:31], v[44:47], v[40:43]
	v_mfma_i32_16x16x64_i8 v[44:47], v[16:19], v[48:51], 0
	v_mfma_i32_16x16x64_i8 v[48:51], v[24:27], v[48:51], 0
	v_mfma_i32_16x16x64_i8 v[44:47], v[20:23], v[52:55], v[44:47]
	v_mfma_i32_16x16x64_i8 v[48:51], v[28:31], v[52:55], v[48:51]
	v_mfma_i32_16x16x64_i8 v[52:55], v[16:19], v[56:59], 0
	v_mfma_i32_16x16x64_i8 v[56:59], v[24:27], v[56:59], 0
	v_mfma_i32_16x16x64_i8 v[52:55], v[20:23], v[60:63], v[52:55]
	v_mfma_i32_16x16x64_i8 v[56:59], v[28:31], v[60:63], v[56:59]
	s_barrier
	ds_read_b128 v[60:63], v221 offset:16384
	ds_read_b128 v[100:103], v221 offset:17408
	ds_read_b128 v[104:107], v221 offset:18432
	ds_read_b128 v[108:111], v221 offset:19456
	ds_read_b128 v[112:115], v221 offset:20480
	ds_read_b128 v[116:119], v221 offset:21504
	ds_read_b128 v[120:123], v221 offset:22528
	ds_read_b128 v[124:127], v221 offset:23552
	s_add_i32 m0, s59, 0x10000
	s_nop 0
	global_load_lds_dwordx4 v216, s[52:53]
	s_nop 0
	s_add_i32 m0, s59, 0x12000
	s_nop 0
	global_load_lds_dwordx4 v218, s[52:53]
	s_add_u32 s52, s8, 0x40100
	s_addc_u32 s53, s9, 0
	s_add_i32 m0, s59, 0x14000
	s_nop 0
	global_load_lds_dwordx4 v216, s[52:53]
	s_nop 0
	s_add_i32 m0, s59, 0x16000
	s_nop 0
	global_load_lds_dwordx4 v218, s[52:53]
	s_nop 0
	s_add_i32 m0, s59, 0
	s_nop 0
	global_load_lds_dwordx4 v215, s[46:47]
	s_nop 0
	s_add_i32 m0, s59, 0x2000
	s_nop 0
	global_load_lds_dwordx4 v217, s[46:47]
	s_waitcnt vmcnt(8) lgkmcnt(0)
	s_barrier
	v_mfma_i32_16x16x64_i8 v[136:139], v[0:3], v[104:107], 0
	v_mfma_i32_16x16x64_i8 v[228:231], v[4:7], v[108:111], v[136:139]
	v_mfma_i32_16x16x64_i8 v[136:139], v[8:11], v[104:107], 0
	v_mfma_i32_16x16x64_i8 v[128:131], v[0:3], v[60:63], 0
	v_mfma_i32_16x16x64_i8 v[132:135], v[8:11], v[60:63], 0
	v_mfma_i32_16x16x64_i8 v[232:235], v[12:15], v[108:111], v[136:139]
	v_mfma_i32_16x16x64_i8 v[136:139], v[0:3], v[112:115], 0
	v_mfma_i32_16x16x64_i8 v[0:3], v[0:3], v[120:123], 0
	v_mfma_i32_16x16x64_i8 v[128:131], v[4:7], v[100:103], v[128:131]
	v_mfma_i32_16x16x64_i8 v[132:135], v[12:15], v[100:103], v[132:135]
	v_mfma_i32_16x16x64_i8 v[236:239], v[4:7], v[116:119], v[136:139]
	v_mfma_i32_16x16x64_i8 v[136:139], v[8:11], v[112:115], 0
	v_mfma_i32_16x16x64_i8 v[0:3], v[4:7], v[124:127], v[0:3]
	v_mfma_i32_16x16x64_i8 v[4:7], v[8:11], v[120:123], 0
	v_mfma_i32_16x16x64_i8 v[240:243], v[12:15], v[116:119], v[136:139]
	v_mfma_i32_16x16x64_i8 v[4:7], v[12:15], v[124:127], v[4:7]
	v_mfma_i32_16x16x64_i8 v[8:11], v[16:19], v[60:63], 0
	v_mfma_i32_16x16x64_i8 v[12:15], v[24:27], v[60:63], 0
	v_mfma_i32_16x16x64_i8 v[8:11], v[20:23], v[100:103], v[8:11]
	v_mfma_i32_16x16x64_i8 v[12:15], v[28:31], v[100:103], v[12:15]
	v_mfma_i32_16x16x64_i8 v[60:63], v[16:19], v[104:107], 0
	v_mfma_i32_16x16x64_i8 v[100:103], v[24:27], v[104:107], 0
	v_mfma_i32_16x16x64_i8 v[104:107], v[16:19], v[112:115], 0
	v_mfma_i32_16x16x64_i8 v[16:19], v[16:19], v[120:123], 0
	v_mfma_i32_16x16x64_i8 v[60:63], v[20:23], v[108:111], v[60:63]
	v_mfma_i32_16x16x64_i8 v[100:103], v[28:31], v[108:111], v[100:103]
	v_mfma_i32_16x16x64_i8 v[244:247], v[20:23], v[116:119], v[104:107]
	v_mfma_i32_16x16x64_i8 v[104:107], v[24:27], v[112:115], 0
	v_mfma_i32_16x16x64_i8 v[16:19], v[20:23], v[124:127], v[16:19]
	v_mfma_i32_16x16x64_i8 v[20:23], v[24:27], v[120:123], 0
	v_mfma_i32_16x16x64_i8 v[248:251], v[28:31], v[116:119], v[104:107]
	v_mfma_i32_16x16x64_i8 v[20:23], v[28:31], v[124:127], v[20:23]
	s_barrier
	ds_read_b128 v[24:27], v222
	ds_read_b128 v[28:31], v222 offset:1024
	ds_read_b128 v[112:115], v222 offset:2048
	ds_read_b128 v[116:119], v222 offset:3072
	ds_read_b128 v[208:211], v223
	ds_read_b128 v[224:227], v223 offset:1024
	ds_read_b128 v[64:67], v223 offset:2048
	ds_read_b128 v[68:71], v223 offset:3072
	ds_read_b128 v[104:107], v221 offset:32768
	ds_read_b128 v[108:111], v221 offset:33792
	ds_read_b128 v[120:123], v221 offset:34816
	ds_read_b128 v[124:127], v221 offset:35840
	ds_read_b128 v[136:139], v221 offset:36864
	ds_read_b128 v[148:151], v221 offset:37888
	ds_read_b128 v[72:75], v221 offset:38912
	ds_read_b128 v[76:79], v221 offset:39936
	s_add_u32 s12, s12, 0x40100
	s_addc_u32 s13, s13, 0
	s_add_i32 m0, s59, 0x4000
	s_nop 0
	global_load_lds_dwordx4 v215, s[12:13]
	s_nop 0
	s_add_i32 m0, s59, 0x6000
	s_nop 0
	global_load_lds_dwordx4 v217, s[12:13]
	s_waitcnt vmcnt(8) lgkmcnt(0)
	s_barrier
	v_mfma_i32_16x16x64_i8 v[140:143], v[24:27], v[104:107], v[140:143]
	v_mfma_i32_16x16x64_i8 v[80:83], v[24:27], v[136:139], v[80:83]
	v_mfma_i32_16x16x64_i8 v[204:207], v[28:31], v[108:111], v[140:143]
	v_mfma_i32_16x16x64_i8 v[140:143], v[112:115], v[104:107], v[144:147]
	v_mfma_i32_16x16x64_i8 v[172:175], v[28:31], v[148:151], v[80:83]
	v_mfma_i32_16x16x64_i8 v[80:83], v[112:115], v[136:139], v[84:87]
	v_mfma_i32_16x16x64_i8 v[200:203], v[116:119], v[108:111], v[140:143]
	v_mfma_i32_16x16x64_i8 v[140:143], v[24:27], v[120:123], v[152:155]
	v_mfma_i32_16x16x64_i8 v[168:171], v[116:119], v[148:151], v[80:83]
	v_mfma_i32_16x16x64_i8 v[80:83], v[24:27], v[72:75], v[88:91]
	v_mfma_i32_16x16x64_i8 v[188:191], v[28:31], v[124:127], v[140:143]
	v_mfma_i32_16x16x64_i8 v[140:143], v[112:115], v[120:123], v[156:159]
	v_mfma_i32_16x16x64_i8 v[156:159], v[28:31], v[76:79], v[80:83]
	v_mfma_i32_16x16x64_i8 v[80:83], v[112:115], v[72:75], v[92:95]
	v_mfma_i32_16x16x64_i8 v[184:187], v[116:119], v[124:127], v[140:143]
	v_mfma_i32_16x16x64_i8 v[152:155], v[116:119], v[76:79], v[80:83]
	v_mfma_i32_16x16x64_i8 v[32:35], v[64:67], v[104:107], v[32:35]
	v_mfma_i32_16x16x64_i8 v[192:195], v[68:71], v[108:111], v[32:35]
	v_mfma_i32_16x16x64_i8 v[32:35], v[208:211], v[120:123], v[36:39]
	v_mfma_i32_16x16x64_i8 v[180:183], v[224:227], v[124:127], v[32:35]
	v_mfma_i32_16x16x64_i8 v[32:35], v[64:67], v[120:123], v[40:43]
	v_mfma_i32_16x16x64_i8 v[176:179], v[68:71], v[124:127], v[32:35]
	v_mfma_i32_16x16x64_i8 v[32:35], v[208:211], v[136:139], v[44:47]
	v_mfma_i32_16x16x64_i8 v[164:167], v[224:227], v[148:151], v[32:35]
	v_mfma_i32_16x16x64_i8 v[32:35], v[64:67], v[136:139], v[48:51]
	v_mfma_i32_16x16x64_i8 v[160:163], v[68:71], v[148:151], v[32:35]
	v_mfma_i32_16x16x64_i8 v[32:35], v[208:211], v[72:75], v[52:55]
	v_mfma_i32_16x16x64_i8 v[80:83], v[208:211], v[104:107], v[96:99]
	v_mfma_i32_16x16x64_i8 v[148:151], v[224:227], v[76:79], v[32:35]
	v_mfma_i32_16x16x64_i8 v[32:35], v[64:67], v[72:75], v[56:59]
	v_mfma_i32_16x16x64_i8 v[196:199], v[224:227], v[108:111], v[80:83]
	v_mfma_i32_16x16x64_i8 v[144:147], v[68:71], v[76:79], v[32:35]
	s_barrier
	s_nop 3
	ds_read_b128 v[32:35], v221 offset:49152
	ds_read_b128 v[36:39], v221 offset:50176
	ds_read_b128 v[40:43], v221 offset:51200
	ds_read_b128 v[44:47], v221 offset:52224
	ds_read_b128 v[48:51], v221 offset:53248
	ds_read_b128 v[52:55], v221 offset:54272
	ds_read_b128 v[56:59], v221 offset:55296
	ds_read_b128 v[76:79], v221 offset:56320
	s_add_i32 m0, s59, 0x18000
	s_nop 0
	global_load_lds_dwordx4 v216, s[50:51]
	s_nop 0
	s_add_i32 m0, s59, 0x1a000
	s_nop 0
	global_load_lds_dwordx4 v218, s[50:51]
	s_add_u32 s12, s8, 0x40180
	s_addc_u32 s13, s9, 0
	s_add_i32 m0, s59, 0x1c000
	s_nop 0
	global_load_lds_dwordx4 v216, s[12:13]
	s_nop 0
	s_add_i32 m0, s59, 0x1e000
	s_nop 0
	global_load_lds_dwordx4 v218, s[12:13]
	s_nop 0
	s_add_i32 m0, s59, 0x8000
	s_nop 0
	global_load_lds_dwordx4 v215, s[48:49]
	s_nop 0
	s_add_i32 m0, s59, 0xa000
	s_nop 0
	global_load_lds_dwordx4 v217, s[48:49]
	s_waitcnt vmcnt(8) lgkmcnt(0)
	s_barrier
	v_mfma_i32_16x16x64_i8 v[72:75], v[24:27], v[32:35], v[128:131]
	v_mfma_i32_16x16x64_i8 v[140:143], v[28:31], v[36:39], v[72:75]
	v_mfma_i32_16x16x64_i8 v[72:75], v[112:115], v[32:35], v[132:135]
	v_mfma_i32_16x16x64_i8 v[136:139], v[116:119], v[36:39], v[72:75]
	v_mfma_i32_16x16x64_i8 v[72:75], v[24:27], v[40:43], v[228:231]
	v_mfma_i32_16x16x64_i8 v[124:127], v[28:31], v[44:47], v[72:75]
	v_mfma_i32_16x16x64_i8 v[72:75], v[112:115], v[40:43], v[232:235]
	v_mfma_i32_16x16x64_i8 v[120:123], v[116:119], v[44:47], v[72:75]
	v_mfma_i32_16x16x64_i8 v[72:75], v[24:27], v[48:51], v[236:239]
	v_mfma_i32_16x16x64_i8 v[0:3], v[24:27], v[56:59], v[0:3]
	v_mfma_i32_16x16x64_i8 v[108:111], v[28:31], v[52:55], v[72:75]
	v_mfma_i32_16x16x64_i8 v[72:75], v[112:115], v[48:51], v[240:243]
	v_mfma_i32_16x16x64_i8 v[88:91], v[28:31], v[76:79], v[0:3]
	v_mfma_i32_16x16x64_i8 v[0:3], v[112:115], v[56:59], v[4:7]
	v_mfma_i32_16x16x64_i8 v[104:107], v[116:119], v[52:55], v[72:75]
	v_mfma_i32_16x16x64_i8 v[84:87], v[116:119], v[76:79], v[0:3]
	v_mfma_i32_16x16x64_i8 v[0:3], v[208:211], v[32:35], v[8:11]
	v_mfma_i32_16x16x64_i8 v[132:135], v[224:227], v[36:39], v[0:3]
	v_mfma_i32_16x16x64_i8 v[0:3], v[64:67], v[32:35], v[12:15]
	v_mfma_i32_16x16x64_i8 v[128:131], v[68:71], v[36:39], v[0:3]
	v_mfma_i32_16x16x64_i8 v[0:3], v[208:211], v[40:43], v[60:63]
	v_mfma_i32_16x16x64_i8 v[116:119], v[224:227], v[44:47], v[0:3]
	v_mfma_i32_16x16x64_i8 v[0:3], v[64:67], v[40:43], v[100:103]
	v_mfma_i32_16x16x64_i8 v[112:115], v[68:71], v[44:47], v[0:3]
	v_mfma_i32_16x16x64_i8 v[0:3], v[208:211], v[48:51], v[244:247]
	v_mfma_i32_16x16x64_i8 v[100:103], v[224:227], v[52:55], v[0:3]
	v_mfma_i32_16x16x64_i8 v[0:3], v[64:67], v[48:51], v[248:251]
	v_mfma_i32_16x16x64_i8 v[96:99], v[68:71], v[52:55], v[0:3]
	v_mfma_i32_16x16x64_i8 v[0:3], v[208:211], v[56:59], v[16:19]
	v_mfma_i32_16x16x64_i8 v[72:75], v[224:227], v[76:79], v[0:3]
	v_mfma_i32_16x16x64_i8 v[0:3], v[64:67], v[56:59], v[20:23]
	v_mfma_i32_16x16x64_i8 v[68:71], v[68:71], v[76:79], v[0:3]
	s_barrier
	s_add_u32 s77, s8, 0x200
	s_addc_u32 s80, s9, 0
	.p2alignl 6, 3212836864

.LBB0_602:
	s_ashr_i32 s25, s24, 31
	s_lshl_b64 s[26:27], s[24:25], 20
	s_add_u32 s26, s44, s26
	s_addc_u32 s27, s45, s27
	s_and_b64 s[28:29], s[4:5], exec
	s_waitcnt lgkmcnt(0)
	ds_read_b128 v[0:3], v217
	ds_read_b128 v[4:7], v217 offset:1024
	ds_read_b128 v[8:11], v217 offset:2048
	ds_read_b128 v[12:15], v217 offset:3072
	ds_read_b128 v[16:19], v218
	ds_read_b128 v[20:23], v218 offset:1024
	ds_read_b128 v[24:27], v218 offset:2048
	ds_read_b128 v[28:31], v218 offset:3072
	ds_read_b128 v[32:35], v219
	ds_read_b128 v[36:39], v219 offset:1024
	ds_read_b128 v[40:43], v219 offset:2048
	ds_read_b128 v[44:47], v219 offset:3072
	ds_read_b128 v[48:51], v219 offset:4096
	ds_read_b128 v[52:55], v219 offset:5120
	ds_read_b128 v[56:59], v219 offset:6144
	ds_read_b128 v[60:63], v219 offset:7168
	s_cselect_b32 s7, s27, s35
	s_cselect_b32 s9, s26, s34
	s_ashr_i32 s23, s22, 31
	s_lshl_b64 s[28:29], s[22:23], 20
	s_add_u32 s28, s46, s28
	s_addc_u32 s29, s47, s29
	s_and_b64 s[36:37], s[4:5], exec
	s_cselect_b32 s23, s29, s31
	s_cselect_b32 s25, s28, s30
	s_add_u32 s36, s34, 0x100
	s_addc_u32 s37, s35, 0
	s_add_u32 s42, s30, 0x100
	s_addc_u32 s43, s31, 0
	s_add_u32 s38, s34, 0x180
	s_addc_u32 s39, s35, 0
	s_add_u32 s40, s30, 0x180
	s_addc_u32 s41, s31, 0
	s_add_u32 s60, s34, 0x80080
	s_addc_u32 s61, s35, 0
	s_add_i32 m0, s48, 0xc000
	s_nop 0
	global_load_lds_dwordx4 v213, s[60:61]
	s_nop 0
	s_add_i32 m0, s48, 0xe000
	s_nop 0
	global_load_lds_dwordx4 v214, s[60:61]
	s_waitcnt vmcnt(8) lgkmcnt(0)
	s_barrier
	v_mfma_f32_16x16x32_bf16 v[64:67], v[0:3], v[32:35], 0
	v_mfma_f32_16x16x32_bf16 v[68:71], v[8:11], v[32:35], 0
	v_mfma_f32_16x16x32_bf16 v[72:75], v[0:3], v[40:43], 0
	v_mfma_f32_16x16x32_bf16 v[76:79], v[8:11], v[40:43], 0
	v_mfma_f32_16x16x32_bf16 v[80:83], v[0:3], v[48:51], 0
	v_mfma_f32_16x16x32_bf16 v[84:87], v[8:11], v[48:51], 0
	v_mfma_f32_16x16x32_bf16 v[88:91], v[0:3], v[56:59], 0
	v_mfma_f32_16x16x32_bf16 v[64:67], v[4:7], v[36:39], v[64:67]
	v_mfma_f32_16x16x32_bf16 v[68:71], v[12:15], v[36:39], v[68:71]
	v_mfma_f32_16x16x32_bf16 v[72:75], v[4:7], v[44:47], v[72:75]
	v_mfma_f32_16x16x32_bf16 v[76:79], v[12:15], v[44:47], v[76:79]
	v_mfma_f32_16x16x32_bf16 v[80:83], v[4:7], v[52:55], v[80:83]
	v_mfma_f32_16x16x32_bf16 v[84:87], v[12:15], v[52:55], v[84:87]
	v_mfma_f32_16x16x32_bf16 v[96:99], v[4:7], v[60:63], v[88:91]
	v_mfma_f32_16x16x32_bf16 v[88:91], v[8:11], v[56:59], 0
	v_mfma_f32_16x16x32_bf16 v[100:103], v[12:15], v[60:63], v[88:91]
	v_mfma_f32_16x16x32_bf16 v[88:91], v[16:19], v[32:35], 0
	v_mfma_f32_16x16x32_bf16 v[32:35], v[24:27], v[32:35], 0
	v_mfma_f32_16x16x32_bf16 v[104:107], v[20:23], v[36:39], v[88:91]
	v_mfma_f32_16x16x32_bf16 v[32:35], v[28:31], v[36:39], v[32:35]
	v_mfma_f32_16x16x32_bf16 v[36:39], v[16:19], v[40:43], 0
	v_mfma_f32_16x16x32_bf16 v[40:43], v[24:27], v[40:43], 0
	v_mfma_f32_16x16x32_bf16 v[36:39], v[20:23], v[44:47], v[36:39]
	v_mfma_f32_16x16x32_bf16 v[40:43], v[28:31], v[44:47], v[40:43]
	v_mfma_f32_16x16x32_bf16 v[44:47], v[16:19], v[48:51], 0
	v_mfma_f32_16x16x32_bf16 v[48:51], v[24:27], v[48:51], 0
	v_mfma_f32_16x16x32_bf16 v[44:47], v[20:23], v[52:55], v[44:47]
	v_mfma_f32_16x16x32_bf16 v[48:51], v[28:31], v[52:55], v[48:51]
	v_mfma_f32_16x16x32_bf16 v[52:55], v[16:19], v[56:59], 0
	v_mfma_f32_16x16x32_bf16 v[56:59], v[24:27], v[56:59], 0
	v_mfma_f32_16x16x32_bf16 v[52:55], v[20:23], v[60:63], v[52:55]
	v_mfma_f32_16x16x32_bf16 v[56:59], v[28:31], v[60:63], v[56:59]
	s_barrier
	ds_read_b128 v[60:63], v219 offset:16384
	ds_read_b128 v[88:91], v219 offset:17408
	ds_read_b128 v[92:95], v219 offset:18432
	ds_read_b128 v[108:111], v219 offset:19456
	ds_read_b128 v[112:115], v219 offset:20480
	ds_read_b128 v[116:119], v219 offset:21504
	ds_read_b128 v[120:123], v219 offset:22528
	ds_read_b128 v[124:127], v219 offset:23552
	s_add_i32 m0, s48, 0x10000
	s_nop 0
	global_load_lds_dwordx4 v213, s[42:43]
	s_nop 0
	s_add_i32 m0, s48, 0x12000
	s_nop 0
	global_load_lds_dwordx4 v214, s[42:43]
	s_add_u32 s42, s30, 0x80100
	s_addc_u32 s43, s31, 0
	s_add_i32 m0, s48, 0x14000
	s_nop 0
	global_load_lds_dwordx4 v213, s[42:43]
	s_nop 0
	s_add_i32 m0, s48, 0x16000
	s_nop 0
	global_load_lds_dwordx4 v214, s[42:43]
	s_nop 0
	s_add_i32 m0, s48, 0
	s_nop 0
	global_load_lds_dwordx4 v213, s[36:37]
	s_nop 0
	s_add_i32 m0, s48, 0x2000
	s_nop 0
	global_load_lds_dwordx4 v214, s[36:37]
	s_waitcnt vmcnt(8) lgkmcnt(0)
	s_barrier
	v_mfma_f32_16x16x32_bf16 v[128:131], v[0:3], v[60:63], 0
	v_mfma_f32_16x16x32_bf16 v[132:135], v[4:7], v[88:91], v[128:131]
	v_mfma_f32_16x16x32_bf16 v[128:131], v[8:11], v[60:63], 0
	v_mfma_f32_16x16x32_bf16 v[140:143], v[12:15], v[88:91], v[128:131]
	v_mfma_f32_16x16x32_bf16 v[128:131], v[0:3], v[92:95], 0
	v_mfma_f32_16x16x32_bf16 v[148:151], v[4:7], v[108:111], v[128:131]
	v_mfma_f32_16x16x32_bf16 v[128:131], v[8:11], v[92:95], 0
	v_mfma_f32_16x16x32_bf16 v[156:159], v[12:15], v[108:111], v[128:131]
	v_mfma_f32_16x16x32_bf16 v[128:131], v[0:3], v[112:115], 0
	v_mfma_f32_16x16x32_bf16 v[0:3], v[0:3], v[120:123], 0
	v_mfma_f32_16x16x32_bf16 v[160:163], v[4:7], v[116:119], v[128:131]
	v_mfma_f32_16x16x32_bf16 v[0:3], v[4:7], v[124:127], v[0:3]
	v_mfma_f32_16x16x32_bf16 v[4:7], v[8:11], v[120:123], 0
	v_mfma_f32_16x16x32_bf16 v[128:131], v[8:11], v[112:115], 0
	v_mfma_f32_16x16x32_bf16 v[4:7], v[12:15], v[124:127], v[4:7]
	v_mfma_f32_16x16x32_bf16 v[164:167], v[12:15], v[116:119], v[128:131]
	v_mfma_f32_16x16x32_bf16 v[8:11], v[16:19], v[60:63], 0
	v_mfma_f32_16x16x32_bf16 v[168:171], v[20:23], v[88:91], v[8:11]
	v_mfma_f32_16x16x32_bf16 v[8:11], v[24:27], v[60:63], 0
	v_mfma_f32_16x16x32_bf16 v[172:175], v[28:31], v[88:91], v[8:11]
	v_mfma_f32_16x16x32_bf16 v[8:11], v[16:19], v[92:95], 0
	v_mfma_f32_16x16x32_bf16 v[176:179], v[20:23], v[108:111], v[8:11]
	v_mfma_f32_16x16x32_bf16 v[8:11], v[24:27], v[92:95], 0
	v_mfma_f32_16x16x32_bf16 v[108:111], v[28:31], v[108:111], v[8:11]
	v_mfma_f32_16x16x32_bf16 v[8:11], v[16:19], v[112:115], 0
	v_mfma_f32_16x16x32_bf16 v[180:183], v[20:23], v[116:119], v[8:11]
	v_mfma_f32_16x16x32_bf16 v[8:11], v[24:27], v[112:115], 0
	v_mfma_f32_16x16x32_bf16 v[116:119], v[28:31], v[116:119], v[8:11]
	v_mfma_f32_16x16x32_bf16 v[8:11], v[16:19], v[120:123], 0
	v_mfma_f32_16x16x32_bf16 v[184:187], v[20:23], v[124:127], v[8:11]
	v_mfma_f32_16x16x32_bf16 v[8:11], v[24:27], v[120:123], 0
	v_mfma_f32_16x16x32_bf16 v[124:127], v[28:31], v[124:127], v[8:11]
	s_barrier
	s_nop 4
	ds_read_b128 v[8:11], v220
	ds_read_b128 v[12:15], v220 offset:1024
	ds_read_b128 v[16:19], v220 offset:2048
	ds_read_b128 v[20:23], v220 offset:3072
	ds_read_b128 v[194:197], v221
	ds_read_b128 v[198:201], v221 offset:1024
	ds_read_b128 v[202:205], v221 offset:2048
	ds_read_b128 v[206:209], v221 offset:3072
	ds_read_b128 v[24:27], v219 offset:32768
	ds_read_b128 v[28:31], v219 offset:33792
	ds_read_b128 v[60:63], v219 offset:34816
	ds_read_b128 v[224:227], v219 offset:35840
	ds_read_b128 v[228:231], v219 offset:36864
	ds_read_b128 v[232:235], v219 offset:37888
	ds_read_b128 v[236:239], v219 offset:38912
	ds_read_b128 v[240:243], v219 offset:39936
	s_add_u32 s34, s34, 0x80100
	s_addc_u32 s35, s35, 0
	s_add_i32 m0, s48, 0x4000
	s_nop 0
	global_load_lds_dwordx4 v213, s[34:35]
	s_nop 0
	s_add_i32 m0, s48, 0x6000
	s_nop 0
	global_load_lds_dwordx4 v214, s[34:35]
	s_waitcnt vmcnt(8) lgkmcnt(0)
	s_barrier
	v_mfma_f32_16x16x32_bf16 v[64:67], v[8:11], v[24:27], v[64:67]
	v_mfma_f32_16x16x32_bf16 v[152:155], v[12:15], v[28:31], v[64:67]
	v_mfma_f32_16x16x32_bf16 v[64:67], v[16:19], v[24:27], v[68:71]
	v_mfma_f32_16x16x32_bf16 v[144:147], v[20:23], v[28:31], v[64:67]
	v_mfma_f32_16x16x32_bf16 v[64:67], v[8:11], v[60:63], v[72:75]
	v_mfma_f32_16x16x32_bf16 v[120:123], v[12:15], v[224:227], v[64:67]
	v_mfma_f32_16x16x32_bf16 v[64:67], v[16:19], v[60:63], v[76:79]
	v_mfma_f32_16x16x32_bf16 v[112:115], v[20:23], v[224:227], v[64:67]
	v_mfma_f32_16x16x32_bf16 v[64:67], v[8:11], v[228:231], v[80:83]
	v_mfma_f32_16x16x32_bf16 v[92:95], v[12:15], v[232:235], v[64:67]
	v_mfma_f32_16x16x32_bf16 v[64:67], v[16:19], v[228:231], v[84:87]
	v_mfma_f32_16x16x32_bf16 v[88:91], v[20:23], v[232:235], v[64:67]
	v_mfma_f32_16x16x32_bf16 v[64:67], v[8:11], v[236:239], v[96:99]
	v_mfma_f32_16x16x32_bf16 v[76:79], v[12:15], v[240:243], v[64:67]
	v_mfma_f32_16x16x32_bf16 v[64:67], v[16:19], v[236:239], v[100:103]
	v_mfma_f32_16x16x32_bf16 v[72:75], v[20:23], v[240:243], v[64:67]
	v_mfma_f32_16x16x32_bf16 v[64:67], v[194:197], v[24:27], v[104:107]
	v_mfma_f32_16x16x32_bf16 v[24:27], v[202:205], v[24:27], v[32:35]
	v_mfma_f32_16x16x32_bf16 v[128:131], v[206:209], v[28:31], v[24:27]
	v_mfma_f32_16x16x32_bf16 v[24:27], v[194:197], v[60:63], v[36:39]
	v_mfma_f32_16x16x32_bf16 v[104:107], v[198:201], v[224:227], v[24:27]
	v_mfma_f32_16x16x32_bf16 v[24:27], v[202:205], v[60:63], v[40:43]
	v_mfma_f32_16x16x32_bf16 v[96:99], v[206:209], v[224:227], v[24:27]
	v_mfma_f32_16x16x32_bf16 v[24:27], v[194:197], v[228:231], v[44:47]
	v_mfma_f32_16x16x32_bf16 v[84:87], v[198:201], v[232:235], v[24:27]
	v_mfma_f32_16x16x32_bf16 v[24:27], v[202:205], v[228:231], v[48:51]
	v_mfma_f32_16x16x32_bf16 v[80:83], v[206:209], v[232:235], v[24:27]
	v_mfma_f32_16x16x32_bf16 v[24:27], v[194:197], v[236:239], v[52:55]
	v_mfma_f32_16x16x32_bf16 v[68:71], v[198:201], v[240:243], v[24:27]
	v_mfma_f32_16x16x32_bf16 v[24:27], v[202:205], v[236:239], v[56:59]
	v_mfma_f32_16x16x32_bf16 v[136:139], v[198:201], v[28:31], v[64:67]
	v_mfma_f32_16x16x32_bf16 v[64:67], v[206:209], v[240:243], v[24:27]
	s_barrier
	ds_read_b128 v[32:35], v219 offset:49152
	ds_read_b128 v[36:39], v219 offset:50176
	ds_read_b128 v[100:103], v219 offset:51200
	ds_read_b128 v[224:227], v219 offset:52224
	ds_read_b128 v[228:231], v219 offset:53248
	ds_read_b128 v[232:235], v219 offset:54272
	ds_read_b128 v[236:239], v219 offset:55296
	ds_read_b128 v[240:243], v219 offset:56320
	s_add_i32 m0, s48, 0x18000
	s_nop 0
	global_load_lds_dwordx4 v213, s[40:41]
	s_nop 0
	s_add_i32 m0, s48, 0x1a000
	s_nop 0
	global_load_lds_dwordx4 v214, s[40:41]
	s_add_u32 s34, s30, 0x80180
	s_addc_u32 s35, s31, 0
	s_add_i32 m0, s48, 0x1c000
	s_nop 0
	global_load_lds_dwordx4 v213, s[34:35]
	s_nop 0
	s_add_i32 m0, s48, 0x1e000
	s_nop 0
	global_load_lds_dwordx4 v214, s[34:35]
	s_nop 0
	s_add_i32 m0, s48, 0x8000
	s_nop 0
	global_load_lds_dwordx4 v213, s[38:39]
	s_nop 0
	s_add_i32 m0, s48, 0xa000
	s_nop 0
	global_load_lds_dwordx4 v214, s[38:39]
	s_waitcnt vmcnt(8) lgkmcnt(0)
	s_barrier
	v_mfma_f32_16x16x32_bf16 v[24:27], v[8:11], v[32:35], v[132:135]
	v_mfma_f32_16x16x32_bf16 v[60:63], v[12:15], v[36:39], v[24:27]
	v_mfma_f32_16x16x32_bf16 v[24:27], v[16:19], v[32:35], v[140:143]
	v_mfma_f32_16x16x32_bf16 v[56:59], v[20:23], v[36:39], v[24:27]
	v_mfma_f32_16x16x32_bf16 v[24:27], v[8:11], v[100:103], v[148:151]
	v_mfma_f32_16x16x32_bf16 v[44:47], v[12:15], v[224:227], v[24:27]
	v_mfma_f32_16x16x32_bf16 v[24:27], v[16:19], v[100:103], v[156:159]
	v_mfma_f32_16x16x32_bf16 v[40:43], v[20:23], v[224:227], v[24:27]
	v_mfma_f32_16x16x32_bf16 v[24:27], v[8:11], v[228:231], v[160:163]
	v_mfma_f32_16x16x32_bf16 v[0:3], v[8:11], v[236:239], v[0:3]
	v_mfma_f32_16x16x32_bf16 v[28:31], v[12:15], v[232:235], v[24:27]
	v_mfma_f32_16x16x32_bf16 v[24:27], v[16:19], v[228:231], v[164:167]
	v_mfma_f32_16x16x32_bf16 v[12:15], v[12:15], v[240:243], v[0:3]
	v_mfma_f32_16x16x32_bf16 v[0:3], v[16:19], v[236:239], v[4:7]
	v_mfma_f32_16x16x32_bf16 v[24:27], v[20:23], v[232:235], v[24:27]
	v_mfma_f32_16x16x32_bf16 v[8:11], v[20:23], v[240:243], v[0:3]
	v_mfma_f32_16x16x32_bf16 v[0:3], v[194:197], v[32:35], v[168:171]
	v_mfma_f32_16x16x32_bf16 v[52:55], v[198:201], v[36:39], v[0:3]
	v_mfma_f32_16x16x32_bf16 v[0:3], v[202:205], v[32:35], v[172:175]
	v_mfma_f32_16x16x32_bf16 v[48:51], v[206:209], v[36:39], v[0:3]
	v_mfma_f32_16x16x32_bf16 v[0:3], v[194:197], v[100:103], v[176:179]
	v_mfma_f32_16x16x32_bf16 v[36:39], v[198:201], v[224:227], v[0:3]
	v_mfma_f32_16x16x32_bf16 v[0:3], v[202:205], v[100:103], v[108:111]
	v_mfma_f32_16x16x32_bf16 v[32:35], v[206:209], v[224:227], v[0:3]
	v_mfma_f32_16x16x32_bf16 v[0:3], v[194:197], v[228:231], v[180:183]
	v_mfma_f32_16x16x32_bf16 v[20:23], v[198:201], v[232:235], v[0:3]
	v_mfma_f32_16x16x32_bf16 v[0:3], v[202:205], v[228:231], v[116:119]
	v_mfma_f32_16x16x32_bf16 v[16:19], v[206:209], v[232:235], v[0:3]
	v_mfma_f32_16x16x32_bf16 v[0:3], v[194:197], v[236:239], v[184:187]
	v_mfma_f32_16x16x32_bf16 v[4:7], v[198:201], v[240:243], v[0:3]
	v_mfma_f32_16x16x32_bf16 v[0:3], v[202:205], v[236:239], v[124:127]
	v_mfma_f32_16x16x32_bf16 v[0:3], v[206:209], v[240:243], v[0:3]
	s_barrier
	s_add_u32 s59, s30, 0x200
	s_addc_u32 s60, s31, 0
	s_mov_b32 s61, 0
	.p2alignl 6, 3212836864

.LBB0_752:
	s_ashr_i32 s17, s16, 31
	s_lshl_b64 s[18:19], s[16:17], 19
	s_add_u32 s18, s40, s18
	s_addc_u32 s19, s41, s19
	s_and_b64 s[20:21], s[4:5], exec
	s_cselect_b32 s58, s19, s29
	s_cselect_b32 s59, s18, s28
	s_ashr_i32 s15, s14, 31
	s_lshl_b64 s[20:21], s[14:15], 19
	s_add_u32 s20, s42, s20
	s_addc_u32 s21, s43, s21
	s_and_b64 s[26:27], s[4:5], exec
	ds_read_b128 v[0:3], v204 offset:3072
	ds_read_b128 v[4:7], v204 offset:2048
	ds_read_b128 v[8:11], v204 offset:1024
	ds_read_b128 v[12:15], v204
	ds_read_b128 v[16:19], v205 offset:3072
	ds_read_b128 v[20:23], v205 offset:2048
	ds_read_b128 v[24:27], v205 offset:1024
	ds_read_b128 v[28:31], v205
	ds_read_b128 v[32:35], v206
	ds_read_b128 v[36:39], v206 offset:1024
	ds_read_b128 v[40:43], v206 offset:2048
	ds_read_b128 v[44:47], v206 offset:3072
	ds_read_b128 v[48:51], v206 offset:4096
	ds_read_b128 v[52:55], v206 offset:5120
	ds_read_b128 v[56:59], v206 offset:6144
	ds_read_b128 v[60:63], v206 offset:7168
	s_cselect_b32 s15, s21, s25
	s_cselect_b32 s60, s20, s24
	s_lshl_b32 s26, s55, 11
	s_and_b32 s26, s26, 0x800
	s_or_b32 s38, s26, s49
	s_lshl_b64 s[30:31], s[16:17], 11
	s_add_u32 s26, s28, 0x100
	s_addc_u32 s27, s29, 0
	s_add_u32 s62, s24, 0x100
	s_addc_u32 s63, s25, 0
	s_add_u32 s34, s28, 0x180
	s_addc_u32 s35, s29, 0
	s_add_u32 s36, s24, 0x180
	s_addc_u32 s37, s25, 0
	s_add_u32 s66, s28, 0x40080
	s_addc_u32 s67, s29, 0
	s_add_i32 m0, s46, 0xc000
	s_nop 0
	global_load_lds_dwordx4 v199, s[66:67]
	s_nop 0
	s_add_i32 m0, s46, 0xe000
	s_nop 0
	global_load_lds_dwordx4 v201, s[66:67]
	s_waitcnt vmcnt(8) lgkmcnt(0)
	s_barrier
	s_waitcnt lgkmcnt(7)
	v_mfma_i32_16x16x64_i8 v[64:67], v[28:31], v[32:35], 0
	s_mov_b32 s17, 0
	v_mfma_i32_16x16x64_i8 v[68:71], v[20:23], v[32:35], 0
	s_waitcnt lgkmcnt(5)
	v_mfma_i32_16x16x64_i8 v[72:75], v[28:31], v[40:43], 0
	v_mfma_i32_16x16x64_i8 v[132:135], v[24:27], v[36:39], v[64:67]
	v_mfma_i32_16x16x64_i8 v[136:139], v[16:19], v[36:39], v[68:71]
	s_waitcnt lgkmcnt(4)
	v_mfma_i32_16x16x64_i8 v[144:147], v[24:27], v[44:47], v[72:75]
	v_mfma_i32_16x16x64_i8 v[76:79], v[20:23], v[40:43], 0
	s_waitcnt lgkmcnt(3)
	v_mfma_i32_16x16x64_i8 v[80:83], v[28:31], v[48:51], 0
	v_mfma_i32_16x16x64_i8 v[84:87], v[20:23], v[48:51], 0
	s_waitcnt lgkmcnt(1)
	v_mfma_i32_16x16x64_i8 v[88:91], v[28:31], v[56:59], 0
	v_mfma_i32_16x16x64_i8 v[92:95], v[20:23], v[56:59], 0
	v_mfma_i32_16x16x64_i8 v[76:79], v[16:19], v[44:47], v[76:79]
	v_mfma_i32_16x16x64_i8 v[80:83], v[24:27], v[52:55], v[80:83]
	v_mfma_i32_16x16x64_i8 v[84:87], v[16:19], v[52:55], v[84:87]
	s_waitcnt lgkmcnt(0)
	v_mfma_i32_16x16x64_i8 v[88:91], v[24:27], v[60:63], v[88:91]
	v_mfma_i32_16x16x64_i8 v[92:95], v[16:19], v[60:63], v[92:95]
	v_mfma_i32_16x16x64_i8 v[96:99], v[12:15], v[32:35], 0
	v_mfma_i32_16x16x64_i8 v[32:35], v[4:7], v[32:35], 0
	v_mfma_i32_16x16x64_i8 v[96:99], v[8:11], v[36:39], v[96:99]
	v_mfma_i32_16x16x64_i8 v[32:35], v[0:3], v[36:39], v[32:35]
	v_mfma_i32_16x16x64_i8 v[36:39], v[12:15], v[40:43], 0
	v_mfma_i32_16x16x64_i8 v[40:43], v[4:7], v[40:43], 0
	v_mfma_i32_16x16x64_i8 v[36:39], v[8:11], v[44:47], v[36:39]
	v_mfma_i32_16x16x64_i8 v[40:43], v[0:3], v[44:47], v[40:43]
	v_mfma_i32_16x16x64_i8 v[44:47], v[12:15], v[48:51], 0
	v_mfma_i32_16x16x64_i8 v[48:51], v[4:7], v[48:51], 0
	v_mfma_i32_16x16x64_i8 v[44:47], v[8:11], v[52:55], v[44:47]
	v_mfma_i32_16x16x64_i8 v[48:51], v[0:3], v[52:55], v[48:51]
	v_mfma_i32_16x16x64_i8 v[52:55], v[12:15], v[56:59], 0
	v_mfma_i32_16x16x64_i8 v[56:59], v[4:7], v[56:59], 0
	v_mfma_i32_16x16x64_i8 v[52:55], v[8:11], v[60:63], v[52:55]
	v_mfma_i32_16x16x64_i8 v[56:59], v[0:3], v[60:63], v[56:59]
	s_barrier
	ds_read_b128 v[60:63], v206 offset:16384
	ds_read_b128 v[100:103], v206 offset:17408
	ds_read_b128 v[104:107], v206 offset:18432
	ds_read_b128 v[108:111], v206 offset:19456
	ds_read_b128 v[112:115], v206 offset:20480
	ds_read_b128 v[116:119], v206 offset:21504
	ds_read_b128 v[120:123], v206 offset:22528
	ds_read_b128 v[124:127], v206 offset:23552
	s_add_i32 m0, s46, 0x10000
	s_nop 0
	global_load_lds_dwordx4 v200, s[62:63]
	s_nop 0
	s_add_i32 m0, s46, 0x12000
	s_nop 0
	global_load_lds_dwordx4 v202, s[62:63]
	s_add_u32 s62, s24, 0x40100
	s_addc_u32 s63, s25, 0
	s_add_i32 m0, s46, 0x14000
	s_nop 0
	global_load_lds_dwordx4 v200, s[62:63]
	s_nop 0
	s_add_i32 m0, s46, 0x16000
	s_nop 0
	global_load_lds_dwordx4 v202, s[62:63]
	s_nop 0
	s_add_i32 m0, s46, 0
	s_nop 0
	global_load_lds_dwordx4 v199, s[26:27]
	s_nop 0
	s_add_i32 m0, s46, 0x2000
	s_nop 0
	global_load_lds_dwordx4 v201, s[26:27]
	s_waitcnt vmcnt(8) lgkmcnt(0)
	s_barrier
	v_mfma_i32_16x16x64_i8 v[128:131], v[28:31], v[60:63], 0
	v_mfma_i32_16x16x64_i8 v[210:213], v[24:27], v[100:103], v[128:131]
	v_mfma_i32_16x16x64_i8 v[128:131], v[20:23], v[60:63], 0
	v_mfma_i32_16x16x64_i8 v[214:217], v[16:19], v[100:103], v[128:131]
	v_mfma_i32_16x16x64_i8 v[128:131], v[28:31], v[104:107], 0
	v_mfma_i32_16x16x64_i8 v[218:221], v[24:27], v[108:111], v[128:131]
	v_mfma_i32_16x16x64_i8 v[128:131], v[20:23], v[104:107], 0
	v_mfma_i32_16x16x64_i8 v[222:225], v[16:19], v[108:111], v[128:131]
	v_mfma_i32_16x16x64_i8 v[128:131], v[28:31], v[112:115], 0
	v_mfma_i32_16x16x64_i8 v[226:229], v[24:27], v[116:119], v[128:131]
	v_mfma_i32_16x16x64_i8 v[128:131], v[20:23], v[112:115], 0
	v_mfma_i32_16x16x64_i8 v[28:31], v[28:31], v[120:123], 0
	v_mfma_i32_16x16x64_i8 v[20:23], v[20:23], v[120:123], 0
	v_mfma_i32_16x16x64_i8 v[230:233], v[16:19], v[116:119], v[128:131]
	v_mfma_i32_16x16x64_i8 v[24:27], v[24:27], v[124:127], v[28:31]
	v_mfma_i32_16x16x64_i8 v[20:23], v[16:19], v[124:127], v[20:23]
	v_mfma_i32_16x16x64_i8 v[16:19], v[12:15], v[60:63], 0
	v_mfma_i32_16x16x64_i8 v[28:31], v[8:11], v[100:103], v[16:19]
	v_mfma_i32_16x16x64_i8 v[16:19], v[4:7], v[60:63], 0
	v_mfma_i32_16x16x64_i8 v[60:63], v[0:3], v[100:103], v[16:19]
	v_mfma_i32_16x16x64_i8 v[16:19], v[12:15], v[104:107], 0
	v_mfma_i32_16x16x64_i8 v[100:103], v[8:11], v[108:111], v[16:19]
	v_mfma_i32_16x16x64_i8 v[16:19], v[4:7], v[104:107], 0
	v_mfma_i32_16x16x64_i8 v[234:237], v[0:3], v[108:111], v[16:19]
	v_mfma_i32_16x16x64_i8 v[16:19], v[12:15], v[112:115], 0
	v_mfma_i32_16x16x64_i8 v[238:241], v[8:11], v[116:119], v[16:19]
	v_mfma_i32_16x16x64_i8 v[16:19], v[4:7], v[112:115], 0
	v_mfma_i32_16x16x64_i8 v[12:15], v[12:15], v[120:123], 0
	v_mfma_i32_16x16x64_i8 v[4:7], v[4:7], v[120:123], 0
	v_mfma_i32_16x16x64_i8 v[12:15], v[8:11], v[124:127], v[12:15]
	v_mfma_i32_16x16x64_i8 v[4:7], v[0:3], v[124:127], v[4:7]
	v_mfma_i32_16x16x64_i8 v[242:245], v[0:3], v[116:119], v[16:19]
	s_barrier
	ds_read_b128 v[0:3], v207
	ds_read_b128 v[8:11], v207 offset:1024
	ds_read_b128 v[108:111], v207 offset:2048
	ds_read_b128 v[116:119], v207 offset:3072
	ds_read_b128 v[246:249], v208
	ds_read_b128 v[250:253], v208 offset:1024
	ds_read_b128 v[192:195], v208 offset:2048
	ds_read_b128 v[64:67], v208 offset:3072
	ds_read_b128 v[16:19], v206 offset:32768
	ds_read_b128 v[104:107], v206 offset:33792
	ds_read_b128 v[112:115], v206 offset:34816
	ds_read_b128 v[120:123], v206 offset:35840
	ds_read_b128 v[124:127], v206 offset:36864
	ds_read_b128 v[140:143], v206 offset:37888
	ds_read_b128 v[68:71], v206 offset:38912
	ds_read_b128 v[72:75], v206 offset:39936
	s_add_u32 s28, s28, 0x40100
	s_addc_u32 s29, s29, 0
	s_add_i32 m0, s46, 0x4000
	s_nop 0
	global_load_lds_dwordx4 v199, s[28:29]
	s_nop 0
	s_add_i32 m0, s46, 0x6000
	s_nop 0
	global_load_lds_dwordx4 v201, s[28:29]
	s_waitcnt vmcnt(8) lgkmcnt(0)
	s_barrier
	v_mfma_i32_16x16x64_i8 v[76:79], v[108:111], v[112:115], v[76:79]
	v_mfma_i32_16x16x64_i8 v[128:131], v[0:3], v[16:19], v[132:135]
	v_mfma_i32_16x16x64_i8 v[160:163], v[116:119], v[120:123], v[76:79]
	v_mfma_i32_16x16x64_i8 v[76:79], v[0:3], v[124:127], v[80:83]
	v_mfma_i32_16x16x64_i8 v[184:187], v[8:11], v[104:107], v[128:131]
	v_mfma_i32_16x16x64_i8 v[128:131], v[108:111], v[16:19], v[136:139]
	v_mfma_i32_16x16x64_i8 v[152:155], v[8:11], v[140:143], v[76:79]
	v_mfma_i32_16x16x64_i8 v[76:79], v[108:111], v[124:127], v[84:87]
	v_mfma_i32_16x16x64_i8 v[176:179], v[116:119], v[104:107], v[128:131]
	v_mfma_i32_16x16x64_i8 v[128:131], v[0:3], v[112:115], v[144:147]
	v_mfma_i32_16x16x64_i8 v[144:147], v[116:119], v[140:143], v[76:79]
	v_mfma_i32_16x16x64_i8 v[76:79], v[0:3], v[68:71], v[88:91]
	v_mfma_i32_16x16x64_i8 v[136:139], v[8:11], v[72:75], v[76:79]
	v_mfma_i32_16x16x64_i8 v[76:79], v[108:111], v[68:71], v[92:95]
	v_mfma_i32_16x16x64_i8 v[168:171], v[8:11], v[120:123], v[128:131]
	v_mfma_i32_16x16x64_i8 v[128:131], v[116:119], v[72:75], v[76:79]
	v_mfma_i32_16x16x64_i8 v[76:79], v[246:249], v[16:19], v[96:99]
	v_mfma_i32_16x16x64_i8 v[16:19], v[192:195], v[16:19], v[32:35]
	v_mfma_i32_16x16x64_i8 v[180:183], v[64:67], v[104:107], v[16:19]
	v_mfma_i32_16x16x64_i8 v[16:19], v[246:249], v[112:115], v[36:39]
	v_mfma_i32_16x16x64_i8 v[172:175], v[250:253], v[120:123], v[16:19]
	v_mfma_i32_16x16x64_i8 v[16:19], v[192:195], v[112:115], v[40:43]
	v_mfma_i32_16x16x64_i8 v[164:167], v[64:67], v[120:123], v[16:19]
	v_mfma_i32_16x16x64_i8 v[16:19], v[246:249], v[124:127], v[44:47]
	v_mfma_i32_16x16x64_i8 v[156:159], v[250:253], v[140:143], v[16:19]
	v_mfma_i32_16x16x64_i8 v[16:19], v[192:195], v[124:127], v[48:51]
	v_mfma_i32_16x16x64_i8 v[148:151], v[64:67], v[140:143], v[16:19]
	v_mfma_i32_16x16x64_i8 v[16:19], v[246:249], v[68:71], v[52:55]
	v_mfma_i32_16x16x64_i8 v[140:143], v[250:253], v[72:75], v[16:19]
	v_mfma_i32_16x16x64_i8 v[16:19], v[192:195], v[68:71], v[56:59]
	v_mfma_i32_16x16x64_i8 v[188:191], v[250:253], v[104:107], v[76:79]
	v_mfma_i32_16x16x64_i8 v[132:135], v[64:67], v[72:75], v[16:19]
	s_barrier
	ds_read_b128 v[32:35], v206 offset:49152
	ds_read_b128 v[36:39], v206 offset:50176
	ds_read_b128 v[40:43], v206 offset:51200
	ds_read_b128 v[44:47], v206 offset:52224
	ds_read_b128 v[52:55], v206 offset:53248
	ds_read_b128 v[56:59], v206 offset:54272
	ds_read_b128 v[68:71], v206 offset:55296
	ds_read_b128 v[72:75], v206 offset:56320
	s_add_i32 m0, s46, 0x18000
	s_nop 0
	global_load_lds_dwordx4 v200, s[36:37]
	s_nop 0
	s_add_i32 m0, s46, 0x1a000
	s_nop 0
	global_load_lds_dwordx4 v202, s[36:37]
	s_add_u32 s28, s24, 0x40180
	s_addc_u32 s29, s25, 0
	s_add_i32 m0, s46, 0x1c000
	s_nop 0
	global_load_lds_dwordx4 v200, s[28:29]
	s_nop 0
	s_add_i32 m0, s46, 0x1e000
	s_nop 0
	global_load_lds_dwordx4 v202, s[28:29]
	s_nop 0
	s_add_i32 m0, s46, 0x8000
	s_nop 0
	global_load_lds_dwordx4 v199, s[34:35]
	s_nop 0
	s_add_i32 m0, s46, 0xa000
	s_nop 0
	global_load_lds_dwordx4 v201, s[34:35]
	s_waitcnt vmcnt(8) lgkmcnt(0)
	s_barrier
	v_mfma_i32_16x16x64_i8 v[16:19], v[0:3], v[32:35], v[210:213]
	v_mfma_i32_16x16x64_i8 v[120:123], v[8:11], v[36:39], v[16:19]
	v_mfma_i32_16x16x64_i8 v[16:19], v[108:111], v[32:35], v[214:217]
	v_mfma_i32_16x16x64_i8 v[112:115], v[116:119], v[36:39], v[16:19]
	v_mfma_i32_16x16x64_i8 v[16:19], v[0:3], v[40:43], v[218:221]
	v_mfma_i32_16x16x64_i8 v[104:107], v[8:11], v[44:47], v[16:19]
	v_mfma_i32_16x16x64_i8 v[16:19], v[108:111], v[40:43], v[222:225]
	v_mfma_i32_16x16x64_i8 v[96:99], v[116:119], v[44:47], v[16:19]
	v_mfma_i32_16x16x64_i8 v[16:19], v[0:3], v[52:55], v[226:229]
	v_mfma_i32_16x16x64_i8 v[0:3], v[0:3], v[68:71], v[24:27]
	v_mfma_i32_16x16x64_i8 v[48:51], v[8:11], v[56:59], v[16:19]
	v_mfma_i32_16x16x64_i8 v[16:19], v[108:111], v[52:55], v[230:233]
	v_mfma_i32_16x16x64_i8 v[8:11], v[8:11], v[72:75], v[0:3]
	v_mfma_i32_16x16x64_i8 v[0:3], v[108:111], v[68:71], v[20:23]
	v_mfma_i32_16x16x64_i8 v[16:19], v[116:119], v[56:59], v[16:19]
	v_mfma_i32_16x16x64_i8 v[0:3], v[116:119], v[72:75], v[0:3]
	v_mfma_i32_16x16x64_i8 v[20:23], v[246:249], v[32:35], v[28:31]
	v_mfma_i32_16x16x64_i8 v[124:127], v[250:253], v[36:39], v[20:23]
	v_mfma_i32_16x16x64_i8 v[20:23], v[192:195], v[32:35], v[60:63]
	v_mfma_i32_16x16x64_i8 v[116:119], v[64:67], v[36:39], v[20:23]
	v_mfma_i32_16x16x64_i8 v[20:23], v[246:249], v[40:43], v[100:103]
	v_mfma_i32_16x16x64_i8 v[108:111], v[250:253], v[44:47], v[20:23]
	v_mfma_i32_16x16x64_i8 v[20:23], v[192:195], v[40:43], v[234:237]
	v_mfma_i32_16x16x64_i8 v[100:103], v[64:67], v[44:47], v[20:23]
	v_mfma_i32_16x16x64_i8 v[20:23], v[246:249], v[52:55], v[238:241]
	v_mfma_i32_16x16x64_i8 v[60:63], v[250:253], v[56:59], v[20:23]
	v_mfma_i32_16x16x64_i8 v[20:23], v[192:195], v[52:55], v[242:245]
	v_mfma_i32_16x16x64_i8 v[12:15], v[246:249], v[68:71], v[12:15]
	v_mfma_i32_16x16x64_i8 v[4:7], v[192:195], v[68:71], v[4:7]
	v_mfma_i32_16x16x64_i8 v[44:47], v[64:67], v[56:59], v[20:23]
	v_mfma_i32_16x16x64_i8 v[12:15], v[250:253], v[72:75], v[12:15]
	v_mfma_i32_16x16x64_i8 v[4:7], v[64:67], v[72:75], v[4:7]
	s_barrier
	s_add_u32 s28, s44, s30
	s_addc_u32 s29, s45, s31
	s_add_u32 s61, s24, 0x200
	s_addc_u32 s62, s25, 0
	s_add_i32 s63, s38, 0
	s_add_i32 s63, s63, 0x20000
	.p2alignl 6, 3212836864

.LBB0_837:
	s_waitcnt lgkmcnt(0)
	ds_read_b128 v[0:3], v181
	ds_read_b128 v[4:7], v181 offset:1024
	ds_read_b128 v[8:11], v181 offset:2048
	ds_read_b128 v[12:15], v181 offset:3072
	ds_read_b128 v[16:19], v182
	ds_read_b128 v[20:23], v182 offset:1024
	ds_read_b128 v[24:27], v182 offset:2048
	ds_read_b128 v[28:31], v182 offset:3072
	ds_read_b128 v[32:35], v183
	ds_read_b128 v[36:39], v183 offset:1024
	ds_read_b128 v[40:43], v183 offset:2048
	ds_read_b128 v[44:47], v183 offset:3072
	ds_read_b128 v[48:51], v183 offset:4096
	ds_read_b128 v[52:55], v183 offset:5120
	ds_read_b128 v[56:59], v183 offset:6144
	ds_read_b128 v[60:63], v183 offset:7168
	s_add_u32 s28, s22, 0x100
	s_addc_u32 s29, s23, 0
	s_add_u32 s52, s24, 0x100
	s_addc_u32 s53, s25, 0
	s_add_u32 s6, s22, 0x180
	s_addc_u32 s7, s23, 0
	s_add_u32 s26, s24, 0x180
	s_addc_u32 s27, s25, 0
	s_add_u32 s54, s22, 0x160080
	s_addc_u32 s55, s23, 0
	s_add_i32 m0, s36, 0xc000
	s_nop 0
	global_load_lds_dwordx4 v175, s[54:55]
	s_nop 0
	s_add_i32 m0, s36, 0xe000
	s_nop 0
	global_load_lds_dwordx4 v177, s[54:55]
	s_waitcnt vmcnt(8) lgkmcnt(0)
	s_barrier
	v_mfma_f32_16x16x32_bf16 v[88:91], v[0:3], v[56:59], 0
	v_mfma_f32_16x16x32_bf16 v[64:67], v[0:3], v[32:35], 0
	v_mfma_f32_16x16x32_bf16 v[68:71], v[8:11], v[32:35], 0
	v_mfma_f32_16x16x32_bf16 v[72:75], v[0:3], v[40:43], 0
	v_mfma_f32_16x16x32_bf16 v[76:79], v[8:11], v[40:43], 0
	v_mfma_f32_16x16x32_bf16 v[80:83], v[0:3], v[48:51], 0
	v_mfma_f32_16x16x32_bf16 v[84:87], v[8:11], v[48:51], 0
	v_mfma_f32_16x16x32_bf16 v[96:99], v[4:7], v[60:63], v[88:91]
	v_mfma_f32_16x16x32_bf16 v[88:91], v[8:11], v[56:59], 0
	v_mfma_f32_16x16x32_bf16 v[64:67], v[4:7], v[36:39], v[64:67]
	v_mfma_f32_16x16x32_bf16 v[68:71], v[12:15], v[36:39], v[68:71]
	v_mfma_f32_16x16x32_bf16 v[72:75], v[4:7], v[44:47], v[72:75]
	v_mfma_f32_16x16x32_bf16 v[76:79], v[12:15], v[44:47], v[76:79]
	v_mfma_f32_16x16x32_bf16 v[80:83], v[4:7], v[52:55], v[80:83]
	v_mfma_f32_16x16x32_bf16 v[84:87], v[12:15], v[52:55], v[84:87]
	v_mfma_f32_16x16x32_bf16 v[100:103], v[12:15], v[60:63], v[88:91]
	v_mfma_f32_16x16x32_bf16 v[88:91], v[16:19], v[32:35], 0
	v_mfma_f32_16x16x32_bf16 v[32:35], v[24:27], v[32:35], 0
	v_mfma_f32_16x16x32_bf16 v[112:115], v[20:23], v[36:39], v[88:91]
	v_mfma_f32_16x16x32_bf16 v[32:35], v[28:31], v[36:39], v[32:35]
	v_mfma_f32_16x16x32_bf16 v[36:39], v[16:19], v[40:43], 0
	v_mfma_f32_16x16x32_bf16 v[40:43], v[24:27], v[40:43], 0
	v_mfma_f32_16x16x32_bf16 v[36:39], v[20:23], v[44:47], v[36:39]
	v_mfma_f32_16x16x32_bf16 v[40:43], v[28:31], v[44:47], v[40:43]
	v_mfma_f32_16x16x32_bf16 v[44:47], v[16:19], v[48:51], 0
	v_mfma_f32_16x16x32_bf16 v[48:51], v[24:27], v[48:51], 0
	v_mfma_f32_16x16x32_bf16 v[44:47], v[20:23], v[52:55], v[44:47]
	v_mfma_f32_16x16x32_bf16 v[48:51], v[28:31], v[52:55], v[48:51]
	v_mfma_f32_16x16x32_bf16 v[52:55], v[16:19], v[56:59], 0
	v_mfma_f32_16x16x32_bf16 v[56:59], v[24:27], v[56:59], 0
	v_mfma_f32_16x16x32_bf16 v[52:55], v[20:23], v[60:63], v[52:55]
	v_mfma_f32_16x16x32_bf16 v[56:59], v[28:31], v[60:63], v[56:59]
	s_barrier
	ds_read_b128 v[60:63], v183 offset:16384
	ds_read_b128 v[88:91], v183 offset:17408
	ds_read_b128 v[92:95], v183 offset:18432
	ds_read_b128 v[104:107], v183 offset:19456
	ds_read_b128 v[108:111], v183 offset:20480
	ds_read_b128 v[116:119], v183 offset:21504
	ds_read_b128 v[120:123], v183 offset:22528
	ds_read_b128 v[124:127], v183 offset:23552
	s_add_i32 m0, s36, 0x10000
	s_nop 0
	global_load_lds_dwordx4 v176, s[52:53]
	s_nop 0
	s_add_i32 m0, s36, 0x12000
	s_nop 0
	global_load_lds_dwordx4 v178, s[52:53]
	s_add_u32 s52, s24, 0x160100
	s_addc_u32 s53, s25, 0
	s_add_i32 m0, s36, 0x14000
	s_nop 0
	global_load_lds_dwordx4 v176, s[52:53]
	s_nop 0
	s_add_i32 m0, s36, 0x16000
	s_nop 0
	global_load_lds_dwordx4 v178, s[52:53]
	s_nop 0
	s_add_i32 m0, s36, 0
	s_nop 0
	global_load_lds_dwordx4 v175, s[28:29]
	s_nop 0
	s_add_i32 m0, s36, 0x2000
	s_nop 0
	global_load_lds_dwordx4 v177, s[28:29]
	s_waitcnt vmcnt(8) lgkmcnt(0)
	s_barrier
	v_mfma_f32_16x16x32_bf16 v[128:131], v[0:3], v[60:63], 0
	v_mfma_f32_16x16x32_bf16 v[136:139], v[4:7], v[88:91], v[128:131]
	v_mfma_f32_16x16x32_bf16 v[128:131], v[8:11], v[60:63], 0
	v_mfma_f32_16x16x32_bf16 v[140:143], v[12:15], v[88:91], v[128:131]
	v_mfma_f32_16x16x32_bf16 v[128:131], v[0:3], v[92:95], 0
	v_mfma_f32_16x16x32_bf16 v[144:147], v[4:7], v[104:107], v[128:131]
	v_mfma_f32_16x16x32_bf16 v[128:131], v[8:11], v[92:95], 0
	v_mfma_f32_16x16x32_bf16 v[148:151], v[12:15], v[104:107], v[128:131]
	v_mfma_f32_16x16x32_bf16 v[128:131], v[0:3], v[108:111], 0
	v_mfma_f32_16x16x32_bf16 v[0:3], v[0:3], v[120:123], 0
	v_mfma_f32_16x16x32_bf16 v[156:159], v[4:7], v[116:119], v[128:131]
	v_mfma_f32_16x16x32_bf16 v[0:3], v[4:7], v[124:127], v[0:3]
	v_mfma_f32_16x16x32_bf16 v[4:7], v[8:11], v[120:123], 0
	v_mfma_f32_16x16x32_bf16 v[128:131], v[8:11], v[108:111], 0
	v_mfma_f32_16x16x32_bf16 v[4:7], v[12:15], v[124:127], v[4:7]
	v_mfma_f32_16x16x32_bf16 v[160:163], v[12:15], v[116:119], v[128:131]
	v_mfma_f32_16x16x32_bf16 v[8:11], v[16:19], v[60:63], 0
	v_mfma_f32_16x16x32_bf16 v[164:167], v[20:23], v[88:91], v[8:11]
	v_mfma_f32_16x16x32_bf16 v[8:11], v[24:27], v[60:63], 0
	v_mfma_f32_16x16x32_bf16 v[168:171], v[28:31], v[88:91], v[8:11]
	v_mfma_f32_16x16x32_bf16 v[8:11], v[16:19], v[92:95], 0
	v_mfma_f32_16x16x32_bf16 v[188:191], v[20:23], v[104:107], v[8:11]
	v_mfma_f32_16x16x32_bf16 v[8:11], v[24:27], v[92:95], 0
	v_mfma_f32_16x16x32_bf16 v[192:195], v[28:31], v[104:107], v[8:11]
	v_mfma_f32_16x16x32_bf16 v[8:11], v[16:19], v[108:111], 0
	v_mfma_f32_16x16x32_bf16 v[196:199], v[20:23], v[116:119], v[8:11]
	v_mfma_f32_16x16x32_bf16 v[8:11], v[24:27], v[108:111], 0
	v_mfma_f32_16x16x32_bf16 v[116:119], v[28:31], v[116:119], v[8:11]
	v_mfma_f32_16x16x32_bf16 v[8:11], v[16:19], v[120:123], 0
	v_mfma_f32_16x16x32_bf16 v[200:203], v[20:23], v[124:127], v[8:11]
	v_mfma_f32_16x16x32_bf16 v[8:11], v[24:27], v[120:123], 0
	v_mfma_f32_16x16x32_bf16 v[204:207], v[28:31], v[124:127], v[8:11]
	s_barrier
	s_nop 4
	ds_read_b128 v[8:11], v184
	ds_read_b128 v[12:15], v184 offset:1024
	ds_read_b128 v[16:19], v184 offset:2048
	ds_read_b128 v[20:23], v184 offset:3072
	ds_read_b128 v[208:211], v185
	ds_read_b128 v[212:215], v185 offset:1024
	ds_read_b128 v[216:219], v185 offset:2048
	ds_read_b128 v[220:223], v185 offset:3072
	ds_read_b128 v[24:27], v183 offset:32768
	ds_read_b128 v[28:31], v183 offset:33792
	ds_read_b128 v[60:63], v183 offset:34816
	ds_read_b128 v[224:227], v183 offset:35840
	ds_read_b128 v[228:231], v183 offset:36864
	ds_read_b128 v[232:235], v183 offset:37888
	ds_read_b128 v[236:239], v183 offset:38912
	ds_read_b128 v[240:243], v183 offset:39936
	s_add_u32 s28, s22, 0x160100
	s_addc_u32 s29, s23, 0
	s_add_i32 m0, s36, 0x4000
	s_nop 0
	global_load_lds_dwordx4 v175, s[28:29]
	s_nop 0
	s_add_i32 m0, s36, 0x6000
	s_nop 0
	global_load_lds_dwordx4 v177, s[28:29]
	s_waitcnt vmcnt(8) lgkmcnt(0)
	s_barrier
	v_mfma_f32_16x16x32_bf16 v[64:67], v[8:11], v[24:27], v[64:67]
	v_mfma_f32_16x16x32_bf16 v[132:135], v[12:15], v[28:31], v[64:67]
	v_mfma_f32_16x16x32_bf16 v[64:67], v[16:19], v[24:27], v[68:71]
	v_mfma_f32_16x16x32_bf16 v[128:131], v[20:23], v[28:31], v[64:67]
	v_mfma_f32_16x16x32_bf16 v[64:67], v[8:11], v[60:63], v[72:75]
	v_mfma_f32_16x16x32_bf16 v[108:111], v[12:15], v[224:227], v[64:67]
	v_mfma_f32_16x16x32_bf16 v[64:67], v[16:19], v[60:63], v[76:79]
	v_mfma_f32_16x16x32_bf16 v[104:107], v[20:23], v[224:227], v[64:67]
	v_mfma_f32_16x16x32_bf16 v[64:67], v[8:11], v[228:231], v[80:83]
	v_mfma_f32_16x16x32_bf16 v[92:95], v[12:15], v[232:235], v[64:67]
	v_mfma_f32_16x16x32_bf16 v[64:67], v[16:19], v[228:231], v[84:87]
	v_mfma_f32_16x16x32_bf16 v[88:91], v[20:23], v[232:235], v[64:67]
	v_mfma_f32_16x16x32_bf16 v[64:67], v[8:11], v[236:239], v[96:99]
	v_mfma_f32_16x16x32_bf16 v[76:79], v[12:15], v[240:243], v[64:67]
	v_mfma_f32_16x16x32_bf16 v[64:67], v[16:19], v[236:239], v[100:103]
	v_mfma_f32_16x16x32_bf16 v[72:75], v[20:23], v[240:243], v[64:67]
	v_mfma_f32_16x16x32_bf16 v[64:67], v[208:211], v[24:27], v[112:115]
	v_mfma_f32_16x16x32_bf16 v[24:27], v[216:219], v[24:27], v[32:35]
	v_mfma_f32_16x16x32_bf16 v[120:123], v[220:223], v[28:31], v[24:27]
	v_mfma_f32_16x16x32_bf16 v[24:27], v[208:211], v[60:63], v[36:39]
	v_mfma_f32_16x16x32_bf16 v[100:103], v[212:215], v[224:227], v[24:27]
	v_mfma_f32_16x16x32_bf16 v[24:27], v[216:219], v[60:63], v[40:43]
	v_mfma_f32_16x16x32_bf16 v[96:99], v[220:223], v[224:227], v[24:27]
	v_mfma_f32_16x16x32_bf16 v[24:27], v[208:211], v[228:231], v[44:47]
	v_mfma_f32_16x16x32_bf16 v[84:87], v[212:215], v[232:235], v[24:27]
	v_mfma_f32_16x16x32_bf16 v[24:27], v[216:219], v[228:231], v[48:51]
	v_mfma_f32_16x16x32_bf16 v[80:83], v[220:223], v[232:235], v[24:27]
	v_mfma_f32_16x16x32_bf16 v[24:27], v[208:211], v[236:239], v[52:55]
	v_mfma_f32_16x16x32_bf16 v[68:71], v[212:215], v[240:243], v[24:27]
	v_mfma_f32_16x16x32_bf16 v[24:27], v[216:219], v[236:239], v[56:59]
	v_mfma_f32_16x16x32_bf16 v[124:127], v[212:215], v[28:31], v[64:67]
	v_mfma_f32_16x16x32_bf16 v[64:67], v[220:223], v[240:243], v[24:27]
	s_barrier
	ds_read_b128 v[32:35], v183 offset:49152
	ds_read_b128 v[36:39], v183 offset:50176
	ds_read_b128 v[112:115], v183 offset:51200
	ds_read_b128 v[224:227], v183 offset:52224
	ds_read_b128 v[228:231], v183 offset:53248
	ds_read_b128 v[232:235], v183 offset:54272
	ds_read_b128 v[236:239], v183 offset:55296
	ds_read_b128 v[240:243], v183 offset:56320
	s_add_i32 m0, s36, 0x18000
	s_nop 0
	global_load_lds_dwordx4 v176, s[26:27]
	s_nop 0
	s_add_i32 m0, s36, 0x1a000
	s_nop 0
	global_load_lds_dwordx4 v178, s[26:27]
	s_add_u32 s26, s24, 0x160180
	s_addc_u32 s27, s25, 0
	s_add_i32 m0, s36, 0x1c000
	s_nop 0
	global_load_lds_dwordx4 v176, s[26:27]
	s_nop 0
	s_add_i32 m0, s36, 0x1e000
	s_nop 0
	global_load_lds_dwordx4 v178, s[26:27]
	s_nop 0
	s_add_i32 m0, s36, 0x8000
	s_nop 0
	global_load_lds_dwordx4 v175, s[6:7]
	s_nop 0
	s_add_i32 m0, s36, 0xa000
	s_nop 0
	global_load_lds_dwordx4 v177, s[6:7]
	s_waitcnt vmcnt(8) lgkmcnt(0)
	s_barrier
	v_mfma_f32_16x16x32_bf16 v[24:27], v[8:11], v[32:35], v[136:139]
	v_mfma_f32_16x16x32_bf16 v[60:63], v[12:15], v[36:39], v[24:27]
	v_mfma_f32_16x16x32_bf16 v[24:27], v[16:19], v[32:35], v[140:143]
	v_mfma_f32_16x16x32_bf16 v[56:59], v[20:23], v[36:39], v[24:27]
	v_mfma_f32_16x16x32_bf16 v[24:27], v[8:11], v[112:115], v[144:147]
	v_mfma_f32_16x16x32_bf16 v[44:47], v[12:15], v[224:227], v[24:27]
	v_mfma_f32_16x16x32_bf16 v[24:27], v[16:19], v[112:115], v[148:151]
	v_mfma_f32_16x16x32_bf16 v[40:43], v[20:23], v[224:227], v[24:27]
	v_mfma_f32_16x16x32_bf16 v[24:27], v[8:11], v[228:231], v[156:159]
	v_mfma_f32_16x16x32_bf16 v[0:3], v[8:11], v[236:239], v[0:3]
	v_mfma_f32_16x16x32_bf16 v[28:31], v[12:15], v[232:235], v[24:27]
	v_mfma_f32_16x16x32_bf16 v[24:27], v[16:19], v[228:231], v[160:163]
	v_mfma_f32_16x16x32_bf16 v[12:15], v[12:15], v[240:243], v[0:3]
	v_mfma_f32_16x16x32_bf16 v[0:3], v[16:19], v[236:239], v[4:7]
	v_mfma_f32_16x16x32_bf16 v[24:27], v[20:23], v[232:235], v[24:27]
	v_mfma_f32_16x16x32_bf16 v[8:11], v[20:23], v[240:243], v[0:3]
	v_mfma_f32_16x16x32_bf16 v[0:3], v[208:211], v[32:35], v[164:167]
	v_mfma_f32_16x16x32_bf16 v[52:55], v[212:215], v[36:39], v[0:3]
	v_mfma_f32_16x16x32_bf16 v[0:3], v[216:219], v[32:35], v[168:171]
	v_mfma_f32_16x16x32_bf16 v[48:51], v[220:223], v[36:39], v[0:3]
	v_mfma_f32_16x16x32_bf16 v[0:3], v[208:211], v[112:115], v[188:191]
	v_mfma_f32_16x16x32_bf16 v[36:39], v[212:215], v[224:227], v[0:3]
	v_mfma_f32_16x16x32_bf16 v[0:3], v[216:219], v[112:115], v[192:195]
	v_mfma_f32_16x16x32_bf16 v[32:35], v[220:223], v[224:227], v[0:3]
	v_mfma_f32_16x16x32_bf16 v[0:3], v[208:211], v[228:231], v[196:199]
	v_mfma_f32_16x16x32_bf16 v[20:23], v[212:215], v[232:235], v[0:3]
	v_mfma_f32_16x16x32_bf16 v[0:3], v[216:219], v[228:231], v[116:119]
	v_mfma_f32_16x16x32_bf16 v[16:19], v[220:223], v[232:235], v[0:3]
	v_mfma_f32_16x16x32_bf16 v[0:3], v[208:211], v[236:239], v[200:203]
	v_mfma_f32_16x16x32_bf16 v[4:7], v[212:215], v[240:243], v[0:3]
	v_mfma_f32_16x16x32_bf16 v[0:3], v[216:219], v[236:239], v[204:207]
	v_mfma_f32_16x16x32_bf16 v[0:3], v[220:223], v[240:243], v[0:3]
	s_barrier
	s_add_u32 s51, s22, 0x200
	s_addc_u32 s52, s23, 0
	s_add_u32 s53, s24, 0x200
	s_addc_u32 s54, s25, 0
	s_add_u32 s6, s22, 0x160180
	s_addc_u32 s7, s23, 0
	s_mov_b32 s55, 0
	.p2alignl 6, 3212836864

.LBB0_930:
	s_ashr_i32 s37, s36, 31
	s_lshl_b64 s[38:39], s[36:37], 19
	s_add_u32 s38, s19, s38
	s_addc_u32 s39, s21, s39
	s_and_b64 s[40:41], s[4:5], exec
	s_cselect_b32 s9, s39, s45
	s_cselect_b32 s76, s38, s44
	s_ashr_i32 s35, s34, 31
	s_lshl_b64 s[40:41], s[34:35], 19
	s_add_u32 s40, s23, s40
	s_addc_u32 s41, s25, s41
	s_and_b64 s[46:47], s[4:5], exec
	ds_read_b128 v[0:3], v226 offset:3072
	ds_read_b128 v[4:7], v226 offset:2048
	ds_read_b128 v[8:11], v226 offset:1024
	ds_read_b128 v[12:15], v226
	ds_read_b128 v[16:19], v227 offset:3072
	ds_read_b128 v[20:23], v227 offset:2048
	ds_read_b128 v[24:27], v227 offset:1024
	ds_read_b128 v[28:31], v227
	ds_read_b128 v[32:35], v228
	ds_read_b128 v[36:39], v228 offset:1024
	ds_read_b128 v[40:43], v228 offset:2048
	ds_read_b128 v[44:47], v228 offset:3072
	ds_read_b128 v[48:51], v228 offset:4096
	ds_read_b128 v[52:55], v228 offset:5120
	ds_read_b128 v[56:59], v228 offset:6144
	ds_read_b128 v[60:63], v228 offset:7168
	s_cselect_b32 s35, s41, s43
	s_cselect_b32 s77, s40, s42
	s_lshl_b32 s46, s78, 11
	s_and_b32 s46, s46, 0x800
	s_or_b32 s54, s46, s56
	s_lshl_b64 s[48:49], s[36:37], 11
	s_add_u32 s46, s44, 0x100
	s_addc_u32 s47, s45, 0
	s_add_u32 s80, s42, 0x100
	s_addc_u32 s81, s43, 0
	s_add_u32 s50, s44, 0x180
	s_addc_u32 s51, s45, 0
	s_add_u32 s52, s42, 0x180
	s_addc_u32 s53, s43, 0
	s_add_u32 s82, s44, 0x40080
	s_addc_u32 s83, s45, 0
	s_add_i32 m0, s31, 0xc000
	s_nop 0
	global_load_lds_dwordx4 v219, s[82:83]
	s_nop 0
	s_add_i32 m0, s31, 0xe000
	s_nop 0
	global_load_lds_dwordx4 v221, s[82:83]
	s_waitcnt vmcnt(8) lgkmcnt(0)
	s_barrier
	s_waitcnt lgkmcnt(7)
	v_mfma_i32_16x16x64_i8 v[64:67], v[28:31], v[32:35], 0
	s_mov_b32 s37, 0
	v_mfma_i32_16x16x64_i8 v[68:71], v[20:23], v[32:35], 0
	s_waitcnt lgkmcnt(5)
	v_mfma_i32_16x16x64_i8 v[72:75], v[28:31], v[40:43], 0
	v_mfma_i32_16x16x64_i8 v[76:79], v[20:23], v[40:43], 0
	s_waitcnt lgkmcnt(3)
	v_mfma_i32_16x16x64_i8 v[80:83], v[28:31], v[48:51], 0
	v_mfma_i32_16x16x64_i8 v[84:87], v[20:23], v[48:51], 0
	s_waitcnt lgkmcnt(1)
	v_mfma_i32_16x16x64_i8 v[92:95], v[20:23], v[56:59], 0
	v_mfma_i32_16x16x64_i8 v[136:139], v[24:27], v[36:39], v[64:67]
	v_mfma_i32_16x16x64_i8 v[148:151], v[24:27], v[44:47], v[72:75]
	v_mfma_i32_16x16x64_i8 v[144:147], v[16:19], v[36:39], v[68:71]
	v_mfma_i32_16x16x64_i8 v[76:79], v[16:19], v[44:47], v[76:79]
	v_mfma_i32_16x16x64_i8 v[80:83], v[24:27], v[52:55], v[80:83]
	v_mfma_i32_16x16x64_i8 v[88:91], v[28:31], v[56:59], 0
	v_mfma_i32_16x16x64_i8 v[84:87], v[16:19], v[52:55], v[84:87]
	s_waitcnt lgkmcnt(0)
	v_mfma_i32_16x16x64_i8 v[92:95], v[16:19], v[60:63], v[92:95]
	v_mfma_i32_16x16x64_i8 v[88:91], v[24:27], v[60:63], v[88:91]
	v_mfma_i32_16x16x64_i8 v[96:99], v[12:15], v[32:35], 0
	v_mfma_i32_16x16x64_i8 v[32:35], v[4:7], v[32:35], 0
	v_mfma_i32_16x16x64_i8 v[96:99], v[8:11], v[36:39], v[96:99]
	v_mfma_i32_16x16x64_i8 v[32:35], v[0:3], v[36:39], v[32:35]
	v_mfma_i32_16x16x64_i8 v[36:39], v[12:15], v[40:43], 0
	v_mfma_i32_16x16x64_i8 v[40:43], v[4:7], v[40:43], 0
	v_mfma_i32_16x16x64_i8 v[36:39], v[8:11], v[44:47], v[36:39]
	v_mfma_i32_16x16x64_i8 v[40:43], v[0:3], v[44:47], v[40:43]
	v_mfma_i32_16x16x64_i8 v[44:47], v[12:15], v[48:51], 0
	v_mfma_i32_16x16x64_i8 v[48:51], v[4:7], v[48:51], 0
	v_mfma_i32_16x16x64_i8 v[44:47], v[8:11], v[52:55], v[44:47]
	v_mfma_i32_16x16x64_i8 v[48:51], v[0:3], v[52:55], v[48:51]
	v_mfma_i32_16x16x64_i8 v[52:55], v[12:15], v[56:59], 0
	v_mfma_i32_16x16x64_i8 v[56:59], v[4:7], v[56:59], 0
	v_mfma_i32_16x16x64_i8 v[52:55], v[8:11], v[60:63], v[52:55]
	v_mfma_i32_16x16x64_i8 v[56:59], v[0:3], v[60:63], v[56:59]
	s_barrier
	ds_read_b128 v[60:63], v228 offset:16384
	ds_read_b128 v[100:103], v228 offset:17408
	ds_read_b128 v[104:107], v228 offset:18432
	ds_read_b128 v[108:111], v228 offset:19456
	ds_read_b128 v[112:115], v228 offset:20480
	ds_read_b128 v[116:119], v228 offset:21504
	ds_read_b128 v[120:123], v228 offset:22528
	ds_read_b128 v[124:127], v228 offset:23552
	s_add_i32 m0, s31, 0x10000
	s_nop 0
	global_load_lds_dwordx4 v220, s[80:81]
	s_nop 0
	s_add_i32 m0, s31, 0x12000
	s_nop 0
	global_load_lds_dwordx4 v222, s[80:81]
	s_add_u32 s80, s42, 0x40100
	s_addc_u32 s81, s43, 0
	s_add_i32 m0, s31, 0x14000
	s_nop 0
	global_load_lds_dwordx4 v220, s[80:81]
	s_nop 0
	s_add_i32 m0, s31, 0x16000
	s_nop 0
	global_load_lds_dwordx4 v222, s[80:81]
	s_nop 0
	s_add_i32 m0, s31, 0
	s_nop 0
	global_load_lds_dwordx4 v219, s[46:47]
	s_nop 0
	s_add_i32 m0, s31, 0x2000
	s_nop 0
	global_load_lds_dwordx4 v221, s[46:47]
	s_waitcnt vmcnt(8) lgkmcnt(0)
	s_barrier
	v_mfma_i32_16x16x64_i8 v[132:135], v[20:23], v[60:63], 0
	v_mfma_i32_16x16x64_i8 v[168:171], v[16:19], v[100:103], v[132:135]
	v_mfma_i32_16x16x64_i8 v[132:135], v[28:31], v[104:107], 0
	v_mfma_i32_16x16x64_i8 v[204:207], v[24:27], v[108:111], v[132:135]
	v_mfma_i32_16x16x64_i8 v[132:135], v[20:23], v[104:107], 0
	v_mfma_i32_16x16x64_i8 v[128:131], v[28:31], v[60:63], 0
	v_mfma_i32_16x16x64_i8 v[214:217], v[16:19], v[108:111], v[132:135]
	v_mfma_i32_16x16x64_i8 v[132:135], v[28:31], v[112:115], 0
	v_mfma_i32_16x16x64_i8 v[128:131], v[24:27], v[100:103], v[128:131]
	v_mfma_i32_16x16x64_i8 v[232:235], v[24:27], v[116:119], v[132:135]
	v_mfma_i32_16x16x64_i8 v[132:135], v[20:23], v[112:115], 0
	v_mfma_i32_16x16x64_i8 v[28:31], v[28:31], v[120:123], 0
	v_mfma_i32_16x16x64_i8 v[20:23], v[20:23], v[120:123], 0
	v_mfma_i32_16x16x64_i8 v[236:239], v[16:19], v[116:119], v[132:135]
	v_mfma_i32_16x16x64_i8 v[24:27], v[24:27], v[124:127], v[28:31]
	v_mfma_i32_16x16x64_i8 v[16:19], v[16:19], v[124:127], v[20:23]
	v_mfma_i32_16x16x64_i8 v[20:23], v[12:15], v[60:63], 0
	v_mfma_i32_16x16x64_i8 v[28:31], v[4:7], v[60:63], 0
	v_mfma_i32_16x16x64_i8 v[20:23], v[8:11], v[100:103], v[20:23]
	v_mfma_i32_16x16x64_i8 v[28:31], v[0:3], v[100:103], v[28:31]
	v_mfma_i32_16x16x64_i8 v[60:63], v[12:15], v[104:107], 0
	v_mfma_i32_16x16x64_i8 v[100:103], v[4:7], v[104:107], 0
	v_mfma_i32_16x16x64_i8 v[104:107], v[12:15], v[112:115], 0
	v_mfma_i32_16x16x64_i8 v[100:103], v[0:3], v[108:111], v[100:103]
	v_mfma_i32_16x16x64_i8 v[240:243], v[8:11], v[116:119], v[104:107]
	v_mfma_i32_16x16x64_i8 v[104:107], v[4:7], v[112:115], 0
	v_mfma_i32_16x16x64_i8 v[12:15], v[12:15], v[120:123], 0
	v_mfma_i32_16x16x64_i8 v[4:7], v[4:7], v[120:123], 0
	v_mfma_i32_16x16x64_i8 v[60:63], v[8:11], v[108:111], v[60:63]
	v_mfma_i32_16x16x64_i8 v[244:247], v[0:3], v[116:119], v[104:107]
	v_mfma_i32_16x16x64_i8 v[8:11], v[8:11], v[124:127], v[12:15]
	v_mfma_i32_16x16x64_i8 v[0:3], v[0:3], v[124:127], v[4:7]
	s_barrier
	s_nop 1
	ds_read_b128 v[4:7], v229
	ds_read_b128 v[12:15], v229 offset:1024
	ds_read_b128 v[104:107], v229 offset:2048
	ds_read_b128 v[116:119], v229 offset:3072
	ds_read_b128 v[124:127], v230
	ds_read_b128 v[248:251], v230 offset:1024
	ds_read_b128 v[208:211], v230 offset:2048
	ds_read_b128 v[64:67], v230 offset:3072
	ds_read_b128 v[108:111], v228 offset:32768
	ds_read_b128 v[112:115], v228 offset:33792
	ds_read_b128 v[120:123], v228 offset:34816
	ds_read_b128 v[132:135], v228 offset:35840
	ds_read_b128 v[140:143], v228 offset:36864
	ds_read_b128 v[152:155], v228 offset:37888
	ds_read_b128 v[68:71], v228 offset:38912
	ds_read_b128 v[72:75], v228 offset:39936
	s_add_u32 s44, s44, 0x40100
	s_addc_u32 s45, s45, 0
	s_add_i32 m0, s31, 0x4000
	s_nop 0
	global_load_lds_dwordx4 v219, s[44:45]
	s_nop 0
	s_add_i32 m0, s31, 0x6000
	s_nop 0
	global_load_lds_dwordx4 v221, s[44:45]
	s_waitcnt vmcnt(8) lgkmcnt(0)
	s_barrier
	v_mfma_i32_16x16x64_i8 v[76:79], v[104:107], v[120:123], v[76:79]
	v_mfma_i32_16x16x64_i8 v[180:183], v[116:119], v[132:135], v[76:79]
	v_mfma_i32_16x16x64_i8 v[76:79], v[4:7], v[140:143], v[80:83]
	v_mfma_i32_16x16x64_i8 v[136:139], v[4:7], v[108:111], v[136:139]
	v_mfma_i32_16x16x64_i8 v[164:167], v[12:15], v[152:155], v[76:79]
	v_mfma_i32_16x16x64_i8 v[76:79], v[104:107], v[140:143], v[84:87]
	v_mfma_i32_16x16x64_i8 v[200:203], v[12:15], v[112:115], v[136:139]
	v_mfma_i32_16x16x64_i8 v[136:139], v[104:107], v[108:111], v[144:147]
	v_mfma_i32_16x16x64_i8 v[160:163], v[116:119], v[152:155], v[76:79]
	v_mfma_i32_16x16x64_i8 v[76:79], v[4:7], v[68:71], v[88:91]
	v_mfma_i32_16x16x64_i8 v[196:199], v[116:119], v[112:115], v[136:139]
	v_mfma_i32_16x16x64_i8 v[136:139], v[4:7], v[120:123], v[148:151]
	v_mfma_i32_16x16x64_i8 v[148:151], v[12:15], v[72:75], v[76:79]
	v_mfma_i32_16x16x64_i8 v[76:79], v[104:107], v[68:71], v[92:95]
	v_mfma_i32_16x16x64_i8 v[184:187], v[12:15], v[132:135], v[136:139]
	v_mfma_i32_16x16x64_i8 v[144:147], v[116:119], v[72:75], v[76:79]
	v_mfma_i32_16x16x64_i8 v[32:35], v[208:211], v[108:111], v[32:35]
	v_mfma_i32_16x16x64_i8 v[188:191], v[64:67], v[112:115], v[32:35]
	v_mfma_i32_16x16x64_i8 v[32:35], v[124:127], v[120:123], v[36:39]
	v_mfma_i32_16x16x64_i8 v[176:179], v[248:251], v[132:135], v[32:35]
	v_mfma_i32_16x16x64_i8 v[32:35], v[208:211], v[120:123], v[40:43]
	v_mfma_i32_16x16x64_i8 v[172:175], v[64:67], v[132:135], v[32:35]
	v_mfma_i32_16x16x64_i8 v[32:35], v[124:127], v[140:143], v[44:47]
	v_mfma_i32_16x16x64_i8 v[156:159], v[248:251], v[152:155], v[32:35]
	v_mfma_i32_16x16x64_i8 v[32:35], v[208:211], v[140:143], v[48:51]
	v_mfma_i32_16x16x64_i8 v[152:155], v[64:67], v[152:155], v[32:35]
	v_mfma_i32_16x16x64_i8 v[32:35], v[124:127], v[68:71], v[52:55]
	v_mfma_i32_16x16x64_i8 v[76:79], v[124:127], v[108:111], v[96:99]
	v_mfma_i32_16x16x64_i8 v[140:143], v[248:251], v[72:75], v[32:35]
	v_mfma_i32_16x16x64_i8 v[32:35], v[208:211], v[68:71], v[56:59]
	v_mfma_i32_16x16x64_i8 v[192:195], v[248:251], v[112:115], v[76:79]
	v_mfma_i32_16x16x64_i8 v[136:139], v[64:67], v[72:75], v[32:35]
	s_barrier
	s_nop 3
	ds_read_b128 v[32:35], v228 offset:49152
	ds_read_b128 v[36:39], v228 offset:50176
	ds_read_b128 v[40:43], v228 offset:51200
	ds_read_b128 v[44:47], v228 offset:52224
	ds_read_b128 v[48:51], v228 offset:53248
	ds_read_b128 v[52:55], v228 offset:54272
	ds_read_b128 v[56:59], v228 offset:55296
	ds_read_b128 v[88:91], v228 offset:56320
	s_add_i32 m0, s31, 0x18000
	s_nop 0
	global_load_lds_dwordx4 v220, s[52:53]
	s_nop 0
	s_add_i32 m0, s31, 0x1a000
	s_nop 0
	global_load_lds_dwordx4 v222, s[52:53]
	s_add_u32 s44, s42, 0x40180
	s_addc_u32 s45, s43, 0
	s_add_i32 m0, s31, 0x1c000
	s_nop 0
	global_load_lds_dwordx4 v220, s[44:45]
	s_nop 0
	s_add_i32 m0, s31, 0x1e000
	s_nop 0
	global_load_lds_dwordx4 v222, s[44:45]
	s_nop 0
	s_add_i32 m0, s31, 0x8000
	s_nop 0
	global_load_lds_dwordx4 v219, s[50:51]
	s_nop 0
	s_add_i32 m0, s31, 0xa000
	s_nop 0
	global_load_lds_dwordx4 v221, s[50:51]
	s_waitcnt vmcnt(8) lgkmcnt(0)
	s_barrier
	v_mfma_i32_16x16x64_i8 v[68:71], v[4:7], v[32:35], v[128:131]
	v_mfma_i32_16x16x64_i8 v[132:135], v[12:15], v[36:39], v[68:71]
	v_mfma_i32_16x16x64_i8 v[68:71], v[104:107], v[32:35], v[168:171]
	v_mfma_i32_16x16x64_i8 v[128:131], v[116:119], v[36:39], v[68:71]
	v_mfma_i32_16x16x64_i8 v[68:71], v[4:7], v[40:43], v[204:207]
	v_mfma_i32_16x16x64_i8 v[112:115], v[12:15], v[44:47], v[68:71]
	v_mfma_i32_16x16x64_i8 v[68:71], v[104:107], v[40:43], v[214:217]
	v_mfma_i32_16x16x64_i8 v[108:111], v[116:119], v[44:47], v[68:71]
	v_mfma_i32_16x16x64_i8 v[68:71], v[4:7], v[48:51], v[232:235]
	v_mfma_i32_16x16x64_i8 v[4:7], v[4:7], v[56:59], v[24:27]
	v_mfma_i32_16x16x64_i8 v[96:99], v[12:15], v[52:55], v[68:71]
	v_mfma_i32_16x16x64_i8 v[68:71], v[104:107], v[48:51], v[236:239]
	v_mfma_i32_16x16x64_i8 v[76:79], v[12:15], v[88:91], v[4:7]
	v_mfma_i32_16x16x64_i8 v[4:7], v[104:107], v[56:59], v[16:19]
	v_mfma_i32_16x16x64_i8 v[92:95], v[116:119], v[52:55], v[68:71]
	v_mfma_i32_16x16x64_i8 v[72:75], v[116:119], v[88:91], v[4:7]
	v_mfma_i32_16x16x64_i8 v[4:7], v[124:127], v[32:35], v[20:23]
	v_mfma_i32_16x16x64_i8 v[120:123], v[248:251], v[36:39], v[4:7]
	v_mfma_i32_16x16x64_i8 v[4:7], v[208:211], v[32:35], v[28:31]
	v_mfma_i32_16x16x64_i8 v[116:119], v[64:67], v[36:39], v[4:7]
	v_mfma_i32_16x16x64_i8 v[4:7], v[124:127], v[40:43], v[60:63]
	v_mfma_i32_16x16x64_i8 v[104:107], v[248:251], v[44:47], v[4:7]
	v_mfma_i32_16x16x64_i8 v[4:7], v[208:211], v[40:43], v[100:103]
	v_mfma_i32_16x16x64_i8 v[100:103], v[64:67], v[44:47], v[4:7]
	v_mfma_i32_16x16x64_i8 v[4:7], v[124:127], v[48:51], v[240:243]
	v_mfma_i32_16x16x64_i8 v[84:87], v[248:251], v[52:55], v[4:7]
	v_mfma_i32_16x16x64_i8 v[4:7], v[208:211], v[48:51], v[244:247]
	v_mfma_i32_16x16x64_i8 v[80:83], v[64:67], v[52:55], v[4:7]
	v_mfma_i32_16x16x64_i8 v[4:7], v[124:127], v[56:59], v[8:11]
	v_mfma_i32_16x16x64_i8 v[0:3], v[208:211], v[56:59], v[0:3]
	v_mfma_i32_16x16x64_i8 v[68:71], v[248:251], v[88:91], v[4:7]
	v_mfma_i32_16x16x64_i8 v[64:67], v[64:67], v[88:91], v[0:3]
	s_barrier
	s_add_u32 s44, s27, s48
	s_addc_u32 s45, s29, s49
	s_add_u32 s79, s42, 0x200
	s_addc_u32 s80, s43, 0
	s_add_i32 s81, s54, 0
	s_add_i32 s81, s81, 0x20000
	.p2alignl 6, 3212836864

.LBB0_1108:
	s_ashr_i32 s23, s22, 31
	s_lshl_b64 s[24:25], s[22:23], 20
	s_add_u32 s24, s42, s24
	s_addc_u32 s25, s43, s25
	s_and_b64 s[26:27], s[4:5], exec
	ds_read_b128 v[0:3], v143
	ds_read_b128 v[4:7], v143 offset:1024
	ds_read_b128 v[8:11], v143 offset:2048
	s_waitcnt vmcnt(2)
	ds_read_b128 v[12:15], v143 offset:3072
	s_waitcnt vmcnt(1)
	ds_read_b128 v[16:19], v144
	s_waitcnt vmcnt(0)
	ds_read_b128 v[20:23], v144 offset:1024
	ds_read_b128 v[24:27], v144 offset:2048
	ds_read_b128 v[28:31], v144 offset:3072
	s_cselect_b32 s23, s25, s31
	s_cselect_b32 s51, s24, s30
	s_ashr_i32 s21, s20, 31
	s_lshl_b64 s[26:27], s[20:21], 20
	s_add_u32 s26, s44, s26
	s_addc_u32 s27, s45, s27
	s_and_b64 s[36:37], s[4:5], exec
	s_cselect_b32 s21, s27, s35
	s_cselect_b32 s52, s26, s34
	s_add_u32 s40, s30, 0x100
	s_addc_u32 s41, s31, 0
	s_add_u32 s54, s34, 0x100
	s_addc_u32 s55, s35, 0
	s_add_u32 s36, s30, 0x180
	s_addc_u32 s37, s31, 0
	ds_read_b128 v[32:35], v145
	ds_read_b128 v[36:39], v145 offset:1024
	ds_read_b128 v[40:43], v145 offset:2048
	ds_read_b128 v[44:47], v145 offset:3072
	ds_read_b128 v[48:51], v145 offset:4096
	ds_read_b128 v[52:55], v145 offset:5120
	ds_read_b128 v[56:59], v145 offset:6144
	ds_read_b128 v[60:63], v145 offset:7168
	s_add_u32 s38, s34, 0x180
	s_addc_u32 s39, s35, 0
	s_add_u32 s56, s30, 0x80080
	s_addc_u32 s57, s31, 0
	s_add_i32 m0, s2, 0xc000
	s_nop 0
	global_load_lds_dwordx4 v139, s[56:57]
	s_nop 0
	s_add_i32 m0, s2, 0xe000
	s_nop 0
	global_load_lds_dwordx4 v141, s[56:57]
	s_waitcnt vmcnt(8) lgkmcnt(0)
	s_barrier
	v_mfma_f32_16x16x32_bf16 v[64:67], v[0:3], v[32:35], 0
	v_mfma_f32_16x16x32_bf16 v[68:71], v[8:11], v[32:35], 0
	v_mfma_f32_16x16x32_bf16 v[76:79], v[8:11], v[40:43], 0
	v_mfma_f32_16x16x32_bf16 v[72:75], v[0:3], v[40:43], 0
	v_mfma_f32_16x16x32_bf16 v[80:83], v[0:3], v[48:51], 0
	v_mfma_f32_16x16x32_bf16 v[84:87], v[8:11], v[48:51], 0
	v_mfma_f32_16x16x32_bf16 v[92:95], v[8:11], v[56:59], 0
	v_mfma_f32_16x16x32_bf16 v[88:91], v[0:3], v[56:59], 0
	v_mfma_f32_16x16x32_bf16 v[64:67], v[4:7], v[36:39], v[64:67]
	v_mfma_f32_16x16x32_bf16 v[68:71], v[12:15], v[36:39], v[68:71]
	v_mfma_f32_16x16x32_bf16 v[76:79], v[12:15], v[44:47], v[76:79]
	v_mfma_f32_16x16x32_bf16 v[72:75], v[4:7], v[44:47], v[72:75]
	v_mfma_f32_16x16x32_bf16 v[80:83], v[4:7], v[52:55], v[80:83]
	v_mfma_f32_16x16x32_bf16 v[84:87], v[12:15], v[52:55], v[84:87]
	v_mfma_f32_16x16x32_bf16 v[96:99], v[12:15], v[60:63], v[92:95]
	v_mfma_f32_16x16x32_bf16 v[88:91], v[4:7], v[60:63], v[88:91]
	v_mfma_f32_16x16x32_bf16 v[92:95], v[16:19], v[32:35], 0
	v_mfma_f32_16x16x32_bf16 v[32:35], v[24:27], v[32:35], 0
	v_mfma_f32_16x16x32_bf16 v[104:107], v[20:23], v[36:39], v[92:95]
	v_mfma_f32_16x16x32_bf16 v[32:35], v[28:31], v[36:39], v[32:35]
	v_mfma_f32_16x16x32_bf16 v[36:39], v[16:19], v[40:43], 0
	v_mfma_f32_16x16x32_bf16 v[40:43], v[24:27], v[40:43], 0
	v_mfma_f32_16x16x32_bf16 v[36:39], v[20:23], v[44:47], v[36:39]
	v_mfma_f32_16x16x32_bf16 v[40:43], v[28:31], v[44:47], v[40:43]
	v_mfma_f32_16x16x32_bf16 v[44:47], v[16:19], v[48:51], 0
	v_mfma_f32_16x16x32_bf16 v[48:51], v[24:27], v[48:51], 0
	v_mfma_f32_16x16x32_bf16 v[44:47], v[20:23], v[52:55], v[44:47]
	v_mfma_f32_16x16x32_bf16 v[48:51], v[28:31], v[52:55], v[48:51]
	v_mfma_f32_16x16x32_bf16 v[52:55], v[16:19], v[56:59], 0
	v_mfma_f32_16x16x32_bf16 v[56:59], v[24:27], v[56:59], 0
	v_mfma_f32_16x16x32_bf16 v[52:55], v[20:23], v[60:63], v[52:55]
	v_mfma_f32_16x16x32_bf16 v[60:63], v[28:31], v[60:63], v[56:59]
	s_barrier
	s_nop 3
	ds_read_b128 v[56:59], v145 offset:16384
	ds_read_b128 v[92:95], v145 offset:17408
	ds_read_b128 v[100:103], v145 offset:18432
	ds_read_b128 v[108:111], v145 offset:19456
	ds_read_b128 v[112:115], v145 offset:20480
	ds_read_b128 v[116:119], v145 offset:21504
	ds_read_b128 v[120:123], v145 offset:22528
	ds_read_b128 v[124:127], v145 offset:23552
	s_add_i32 m0, s2, 0x10000
	s_nop 0
	global_load_lds_dwordx4 v140, s[54:55]
	s_nop 0
	s_add_i32 m0, s2, 0x12000
	s_nop 0
	global_load_lds_dwordx4 v142, s[54:55]
	s_add_u32 s54, s34, 0x80100
	s_addc_u32 s55, s35, 0
	s_add_i32 m0, s2, 0x14000
	s_nop 0
	global_load_lds_dwordx4 v140, s[54:55]
	s_nop 0
	s_add_i32 m0, s2, 0x16000
	s_nop 0
	global_load_lds_dwordx4 v142, s[54:55]
	s_nop 0
	s_add_i32 m0, s2, 0
	s_nop 0
	global_load_lds_dwordx4 v139, s[40:41]
	s_nop 0
	s_add_i32 m0, s2, 0x2000
	s_nop 0
	global_load_lds_dwordx4 v141, s[40:41]
	s_waitcnt vmcnt(8) lgkmcnt(0)
	s_barrier
	v_mfma_f32_16x16x32_bf16 v[132:135], v[0:3], v[56:59], 0
	v_mfma_f32_16x16x32_bf16 v[152:155], v[0:3], v[100:103], 0
	v_mfma_f32_16x16x32_bf16 v[160:163], v[0:3], v[112:115], 0
	v_mfma_f32_16x16x32_bf16 v[0:3], v[0:3], v[120:123], 0
	v_mfma_f32_16x16x32_bf16 v[132:135], v[4:7], v[92:95], v[132:135]
	v_mfma_f32_16x16x32_bf16 v[152:155], v[4:7], v[108:111], v[152:155]
	v_mfma_f32_16x16x32_bf16 v[160:163], v[4:7], v[116:119], v[160:163]
	v_mfma_f32_16x16x32_bf16 v[0:3], v[4:7], v[124:127], v[0:3]
	v_mfma_f32_16x16x32_bf16 v[4:7], v[8:11], v[120:123], 0
	v_mfma_f32_16x16x32_bf16 v[148:151], v[8:11], v[56:59], 0
	v_mfma_f32_16x16x32_bf16 v[156:159], v[8:11], v[100:103], 0
	v_mfma_f32_16x16x32_bf16 v[164:167], v[8:11], v[112:115], 0
	v_mfma_f32_16x16x32_bf16 v[4:7], v[12:15], v[124:127], v[4:7]
	v_mfma_f32_16x16x32_bf16 v[148:151], v[12:15], v[92:95], v[148:151]
	v_mfma_f32_16x16x32_bf16 v[156:159], v[12:15], v[108:111], v[156:159]
	v_mfma_f32_16x16x32_bf16 v[164:167], v[12:15], v[116:119], v[164:167]
	v_mfma_f32_16x16x32_bf16 v[12:15], v[24:27], v[56:59], 0
	v_mfma_f32_16x16x32_bf16 v[168:171], v[28:31], v[92:95], v[12:15]
	v_mfma_f32_16x16x32_bf16 v[12:15], v[16:19], v[100:103], 0
	v_mfma_f32_16x16x32_bf16 v[172:175], v[20:23], v[108:111], v[12:15]
	v_mfma_f32_16x16x32_bf16 v[12:15], v[24:27], v[100:103], 0
	v_mfma_f32_16x16x32_bf16 v[176:179], v[28:31], v[108:111], v[12:15]
	v_mfma_f32_16x16x32_bf16 v[12:15], v[16:19], v[112:115], 0
	v_mfma_f32_16x16x32_bf16 v[180:183], v[20:23], v[116:119], v[12:15]
	v_mfma_f32_16x16x32_bf16 v[12:15], v[24:27], v[112:115], 0
	v_mfma_f32_16x16x32_bf16 v[8:11], v[16:19], v[56:59], 0
	v_mfma_f32_16x16x32_bf16 v[184:187], v[28:31], v[116:119], v[12:15]
	v_mfma_f32_16x16x32_bf16 v[12:15], v[16:19], v[120:123], 0
	v_mfma_f32_16x16x32_bf16 v[8:11], v[20:23], v[92:95], v[8:11]
	v_mfma_f32_16x16x32_bf16 v[188:191], v[20:23], v[124:127], v[12:15]
	v_mfma_f32_16x16x32_bf16 v[12:15], v[24:27], v[120:123], 0
	v_mfma_f32_16x16x32_bf16 v[192:195], v[28:31], v[124:127], v[12:15]
	s_barrier
	s_nop 4
	ds_read_b128 v[12:15], v146
	ds_read_b128 v[16:19], v146 offset:1024
	ds_read_b128 v[24:27], v146 offset:2048
	ds_read_b128 v[196:199], v146 offset:3072
	ds_read_b128 v[200:203], v147
	ds_read_b128 v[204:207], v147 offset:1024
	ds_read_b128 v[208:211], v147 offset:2048
	ds_read_b128 v[212:215], v147 offset:3072
	ds_read_b128 v[20:23], v145 offset:32768
	ds_read_b128 v[28:31], v145 offset:33792
	ds_read_b128 v[216:219], v145 offset:34816
	ds_read_b128 v[220:223], v145 offset:35840
	ds_read_b128 v[224:227], v145 offset:36864
	ds_read_b128 v[228:231], v145 offset:37888
	ds_read_b128 v[232:235], v145 offset:38912
	ds_read_b128 v[236:239], v145 offset:39936
	s_add_u32 s40, s30, 0x80100
	s_addc_u32 s41, s31, 0
	s_add_i32 m0, s2, 0x4000
	s_nop 0
	global_load_lds_dwordx4 v139, s[40:41]
	s_nop 0
	s_add_i32 m0, s2, 0x6000
	s_nop 0
	global_load_lds_dwordx4 v141, s[40:41]
	s_waitcnt vmcnt(8) lgkmcnt(0)
	s_barrier
	v_mfma_f32_16x16x32_bf16 v[56:59], v[12:15], v[20:23], v[64:67]
	v_mfma_f32_16x16x32_bf16 v[116:119], v[16:19], v[28:31], v[56:59]
	v_mfma_f32_16x16x32_bf16 v[56:59], v[24:27], v[20:23], v[68:71]
	v_mfma_f32_16x16x32_bf16 v[112:115], v[196:199], v[28:31], v[56:59]
	v_mfma_f32_16x16x32_bf16 v[56:59], v[12:15], v[216:219], v[72:75]
	v_mfma_f32_16x16x32_bf16 v[108:111], v[16:19], v[220:223], v[56:59]
	v_mfma_f32_16x16x32_bf16 v[56:59], v[24:27], v[216:219], v[76:79]
	v_mfma_f32_16x16x32_bf16 v[100:103], v[196:199], v[220:223], v[56:59]
	v_mfma_f32_16x16x32_bf16 v[56:59], v[12:15], v[224:227], v[80:83]
	v_mfma_f32_16x16x32_bf16 v[92:95], v[16:19], v[228:231], v[56:59]
	v_mfma_f32_16x16x32_bf16 v[56:59], v[24:27], v[224:227], v[84:87]
	v_mfma_f32_16x16x32_bf16 v[84:87], v[196:199], v[228:231], v[56:59]
	v_mfma_f32_16x16x32_bf16 v[56:59], v[12:15], v[232:235], v[88:91]
	v_mfma_f32_16x16x32_bf16 v[72:75], v[16:19], v[236:239], v[56:59]
	v_mfma_f32_16x16x32_bf16 v[56:59], v[24:27], v[232:235], v[96:99]
	v_mfma_f32_16x16x32_bf16 v[56:59], v[196:199], v[236:239], v[56:59]
	v_mfma_f32_16x16x32_bf16 v[64:67], v[200:203], v[20:23], v[104:107]
	v_mfma_f32_16x16x32_bf16 v[20:23], v[208:211], v[20:23], v[32:35]
	v_mfma_f32_16x16x32_bf16 v[120:123], v[212:215], v[28:31], v[20:23]
	v_mfma_f32_16x16x32_bf16 v[20:23], v[200:203], v[216:219], v[36:39]
	v_mfma_f32_16x16x32_bf16 v[104:107], v[204:207], v[220:223], v[20:23]
	v_mfma_f32_16x16x32_bf16 v[20:23], v[208:211], v[216:219], v[40:43]
	v_mfma_f32_16x16x32_bf16 v[96:99], v[212:215], v[220:223], v[20:23]
	v_mfma_f32_16x16x32_bf16 v[20:23], v[200:203], v[224:227], v[44:47]
	v_mfma_f32_16x16x32_bf16 v[88:91], v[204:207], v[228:231], v[20:23]
	v_mfma_f32_16x16x32_bf16 v[20:23], v[208:211], v[224:227], v[48:51]
	v_mfma_f32_16x16x32_bf16 v[80:83], v[212:215], v[228:231], v[20:23]
	v_mfma_f32_16x16x32_bf16 v[20:23], v[200:203], v[232:235], v[52:55]
	v_mfma_f32_16x16x32_bf16 v[124:127], v[204:207], v[28:31], v[64:67]
	v_mfma_f32_16x16x32_bf16 v[64:67], v[204:207], v[236:239], v[20:23]
	v_mfma_f32_16x16x32_bf16 v[20:23], v[208:211], v[232:235], v[60:63]
	v_mfma_f32_16x16x32_bf16 v[48:51], v[212:215], v[236:239], v[20:23]
	s_barrier
	ds_read_b128 v[32:35], v145 offset:49152
	ds_read_b128 v[40:43], v145 offset:50176
	ds_read_b128 v[216:219], v145 offset:51200
	ds_read_b128 v[220:223], v145 offset:52224
	ds_read_b128 v[224:227], v145 offset:53248
	ds_read_b128 v[228:231], v145 offset:54272
	ds_read_b128 v[232:235], v145 offset:55296
	ds_read_b128 v[236:239], v145 offset:56320
	s_add_i32 m0, s2, 0x18000
	s_nop 0
	global_load_lds_dwordx4 v140, s[38:39]
	s_nop 0
	s_add_i32 m0, s2, 0x1a000
	s_nop 0
	global_load_lds_dwordx4 v142, s[38:39]
	s_add_u32 s38, s34, 0x80180
	s_addc_u32 s39, s35, 0
	s_add_i32 m0, s2, 0x1c000
	s_nop 0
	global_load_lds_dwordx4 v140, s[38:39]
	s_nop 0
	s_add_i32 m0, s2, 0x1e000
	s_nop 0
	global_load_lds_dwordx4 v142, s[38:39]
	s_nop 0
	s_add_i32 m0, s2, 0x8000
	s_nop 0
	global_load_lds_dwordx4 v139, s[36:37]
	s_nop 0
	s_add_i32 m0, s2, 0xa000
	s_nop 0
	global_load_lds_dwordx4 v141, s[36:37]
	s_waitcnt vmcnt(8) lgkmcnt(0)
	s_barrier
	v_mfma_f32_16x16x32_bf16 v[20:23], v[12:15], v[32:35], v[132:135]
	v_mfma_f32_16x16x32_bf16 v[76:79], v[16:19], v[40:43], v[20:23]
	v_mfma_f32_16x16x32_bf16 v[20:23], v[24:27], v[32:35], v[148:151]
	v_mfma_f32_16x16x32_bf16 v[60:63], v[196:199], v[40:43], v[20:23]
	v_mfma_f32_16x16x32_bf16 v[20:23], v[12:15], v[216:219], v[152:155]
	v_mfma_f32_16x16x32_bf16 v[44:47], v[16:19], v[220:223], v[20:23]
	v_mfma_f32_16x16x32_bf16 v[20:23], v[24:27], v[216:219], v[156:159]
	v_mfma_f32_16x16x32_bf16 v[36:39], v[196:199], v[220:223], v[20:23]
	v_mfma_f32_16x16x32_bf16 v[20:23], v[12:15], v[224:227], v[160:163]
	v_mfma_f32_16x16x32_bf16 v[0:3], v[12:15], v[232:235], v[0:3]
	v_mfma_f32_16x16x32_bf16 v[28:31], v[16:19], v[228:231], v[20:23]
	v_mfma_f32_16x16x32_bf16 v[20:23], v[24:27], v[224:227], v[164:167]
	v_mfma_f32_16x16x32_bf16 v[12:15], v[16:19], v[236:239], v[0:3]
	v_mfma_f32_16x16x32_bf16 v[0:3], v[24:27], v[232:235], v[4:7]
	v_mfma_f32_16x16x32_bf16 v[20:23], v[196:199], v[228:231], v[20:23]
	v_mfma_f32_16x16x32_bf16 v[4:7], v[196:199], v[236:239], v[0:3]
	v_mfma_f32_16x16x32_bf16 v[0:3], v[200:203], v[32:35], v[8:11]
	v_mfma_f32_16x16x32_bf16 v[68:71], v[204:207], v[40:43], v[0:3]
	v_mfma_f32_16x16x32_bf16 v[0:3], v[208:211], v[32:35], v[168:171]
	v_mfma_f32_16x16x32_bf16 v[52:55], v[212:215], v[40:43], v[0:3]
	v_mfma_f32_16x16x32_bf16 v[0:3], v[200:203], v[216:219], v[172:175]
	v_mfma_f32_16x16x32_bf16 v[40:43], v[204:207], v[220:223], v[0:3]
	v_mfma_f32_16x16x32_bf16 v[0:3], v[208:211], v[216:219], v[176:179]
	v_mfma_f32_16x16x32_bf16 v[32:35], v[212:215], v[220:223], v[0:3]
	v_mfma_f32_16x16x32_bf16 v[0:3], v[200:203], v[224:227], v[180:183]
	v_mfma_f32_16x16x32_bf16 v[24:27], v[204:207], v[228:231], v[0:3]
	v_mfma_f32_16x16x32_bf16 v[0:3], v[208:211], v[224:227], v[184:187]
	v_mfma_f32_16x16x32_bf16 v[16:19], v[212:215], v[228:231], v[0:3]
	v_mfma_f32_16x16x32_bf16 v[0:3], v[200:203], v[232:235], v[188:191]
	v_mfma_f32_16x16x32_bf16 v[8:11], v[204:207], v[236:239], v[0:3]
	v_mfma_f32_16x16x32_bf16 v[0:3], v[208:211], v[232:235], v[192:195]
	v_mfma_f32_16x16x32_bf16 v[0:3], v[212:215], v[236:239], v[0:3]
	s_barrier
	s_add_u32 s53, s30, 0x200
	s_addc_u32 s54, s31, 0
	s_add_u32 s55, s34, 0x200
	s_addc_u32 s56, s35, 0
	s_add_u32 s30, s30, 0x80180
	s_addc_u32 s31, s31, 0
	s_mov_b32 s57, 0
	.p2alignl 6, 3212836864

.LBB0_1410:
	ds_read_b128 v[0:3], v138
	ds_read_b128 v[4:7], v138 offset:1024
	ds_read_b128 v[8:11], v138 offset:2048
	ds_read_b128 v[12:15], v138 offset:3072
	ds_read_b128 v[16:19], v139
	ds_read_b128 v[20:23], v139 offset:1024
	ds_read_b128 v[24:27], v139 offset:2048
	ds_read_b128 v[28:31], v139 offset:3072
	ds_read_b128 v[32:35], v140
	ds_read_b128 v[36:39], v140 offset:1024
	ds_read_b128 v[40:43], v140 offset:2048
	ds_read_b128 v[44:47], v140 offset:3072
	ds_read_b128 v[48:51], v140 offset:4096
	ds_read_b128 v[52:55], v140 offset:5120
	ds_read_b128 v[56:59], v140 offset:6144
	ds_read_b128 v[60:63], v140 offset:7168
	s_lshl_b64 s[20:21], s[16:17], 19
	s_add_u32 s20, s39, s20
	s_addc_u32 s21, s40, s21
	s_and_b64 s[6:7], exec, s[6:7]
	s_cselect_b32 s2, s21, s29
	s_cselect_b32 s15, s20, s28
	s_add_u32 s6, s28, 0x100
	s_addc_u32 s7, s29, 0
	s_add_u32 s36, s26, 0x100
	s_addc_u32 s37, s27, 0
	s_add_u32 s30, s28, 0x180
	s_addc_u32 s31, s29, 0
	s_add_u32 s34, s26, 0x180
	s_addc_u32 s35, s27, 0
	s_add_u32 s54, s28, 0x40080
	s_addc_u32 s55, s29, 0
	s_add_i32 m0, s47, 0xc000
	s_nop 0
	global_load_lds_dwordx4 v134, s[54:55]
	s_nop 0
	s_add_i32 m0, s47, 0xe000
	s_nop 0
	global_load_lds_dwordx4 v136, s[54:55]
	s_waitcnt vmcnt(8) lgkmcnt(0)
	s_barrier
	v_mfma_f32_16x16x128_f8f6f4 v[64:67], v[0:7], v[32:39], 0
	v_mfma_f32_16x16x128_f8f6f4 v[68:71], v[8:15], v[32:39], 0
	v_mfma_f32_16x16x128_f8f6f4 v[76:79], v[8:15], v[40:47], 0
	v_mfma_f32_16x16x128_f8f6f4 v[72:75], v[0:7], v[40:47], 0
	v_mfma_f32_16x16x128_f8f6f4 v[80:83], v[0:7], v[48:55], 0
	v_mfma_f32_16x16x128_f8f6f4 v[88:91], v[8:15], v[48:55], 0
	v_mfma_f32_16x16x128_f8f6f4 v[104:107], v[8:15], v[56:63], 0
	v_mfma_f32_16x16x128_f8f6f4 v[92:95], v[0:7], v[56:63], 0
	v_mfma_f32_16x16x128_f8f6f4 v[108:111], v[16:23], v[32:39], 0
	v_mfma_f32_16x16x128_f8f6f4 v[124:127], v[24:31], v[32:39], 0
	v_mfma_f32_16x16x128_f8f6f4 v[166:169], v[24:31], v[40:47], 0
	v_mfma_f32_16x16x128_f8f6f4 v[162:165], v[16:23], v[40:47], 0
	v_mfma_f32_16x16x128_f8f6f4 v[170:173], v[16:23], v[48:55], 0
	v_mfma_f32_16x16x128_f8f6f4 v[174:177], v[24:31], v[48:55], 0
	v_mfma_f32_16x16x128_f8f6f4 v[182:185], v[24:31], v[56:63], 0
	v_mfma_f32_16x16x128_f8f6f4 v[178:181], v[16:23], v[56:63], 0
	s_barrier
	ds_read_b128 v[32:35], v140 offset:16384
	ds_read_b128 v[36:39], v140 offset:17408
	ds_read_b128 v[40:43], v140 offset:18432
	ds_read_b128 v[44:47], v140 offset:19456
	ds_read_b128 v[48:51], v140 offset:20480
	ds_read_b128 v[52:55], v140 offset:21504
	ds_read_b128 v[56:59], v140 offset:22528
	ds_read_b128 v[60:63], v140 offset:23552
	s_add_i32 m0, s47, 0x10000
	s_nop 0
	global_load_lds_dwordx4 v135, s[36:37]
	s_nop 0
	s_add_i32 m0, s47, 0x12000
	s_nop 0
	global_load_lds_dwordx4 v137, s[36:37]
	s_add_u32 s36, s26, 0x40100
	s_addc_u32 s37, s27, 0
	s_add_i32 m0, s47, 0x14000
	s_nop 0
	global_load_lds_dwordx4 v135, s[36:37]
	s_nop 0
	s_add_i32 m0, s47, 0x16000
	s_nop 0
	global_load_lds_dwordx4 v137, s[36:37]
	s_nop 0
	s_add_i32 m0, s47, 0
	s_nop 0
	global_load_lds_dwordx4 v134, s[6:7]
	s_nop 0
	s_add_i32 m0, s47, 0x2000
	s_nop 0
	global_load_lds_dwordx4 v136, s[6:7]
	s_waitcnt vmcnt(8) lgkmcnt(0)
	s_barrier
	v_mfma_f32_16x16x128_f8f6f4 v[186:189], v[0:7], v[32:39], 0
	v_mfma_f32_16x16x128_f8f6f4 v[190:193], v[8:15], v[32:39], 0
	v_mfma_f32_16x16x128_f8f6f4 v[198:201], v[8:15], v[40:47], 0
	v_mfma_f32_16x16x128_f8f6f4 v[194:197], v[0:7], v[40:47], 0
	v_mfma_f32_16x16x128_f8f6f4 v[202:205], v[0:7], v[48:55], 0
	v_mfma_f32_16x16x128_f8f6f4 v[206:209], v[8:15], v[48:55], 0
	v_mfma_f32_16x16x128_f8f6f4 v[214:217], v[8:15], v[56:63], 0
	v_mfma_f32_16x16x128_f8f6f4 v[210:213], v[0:7], v[56:63], 0
	v_mfma_f32_16x16x128_f8f6f4 v[218:221], v[16:23], v[32:39], 0
	v_mfma_f32_16x16x128_f8f6f4 v[222:225], v[24:31], v[32:39], 0
	v_mfma_f32_16x16x128_f8f6f4 v[230:233], v[24:31], v[40:47], 0
	v_mfma_f32_16x16x128_f8f6f4 v[226:229], v[16:23], v[40:47], 0
	v_mfma_f32_16x16x128_f8f6f4 v[234:237], v[16:23], v[48:55], 0
	v_mfma_f32_16x16x128_f8f6f4 v[238:241], v[24:31], v[48:55], 0
	v_mfma_f32_16x16x128_f8f6f4 v[246:249], v[24:31], v[56:63], 0
	v_mfma_f32_16x16x128_f8f6f4 v[242:245], v[16:23], v[56:63], 0
	s_barrier
	ds_read_b128 v[0:3], v141
	ds_read_b128 v[4:7], v141 offset:1024
	ds_read_b128 v[8:11], v141 offset:2048
	ds_read_b128 v[12:15], v141 offset:3072
	ds_read_b128 v[146:149], v142
	ds_read_b128 v[150:153], v142 offset:1024
	ds_read_b128 v[154:157], v142 offset:2048
	ds_read_b128 v[158:161], v142 offset:3072
	ds_read_b128 v[16:19], v140 offset:32768
	ds_read_b128 v[20:23], v140 offset:33792
	ds_read_b128 v[24:27], v140 offset:34816
	ds_read_b128 v[28:31], v140 offset:35840
	ds_read_b128 v[32:35], v140 offset:36864
	ds_read_b128 v[36:39], v140 offset:37888
	ds_read_b128 v[40:43], v140 offset:38912
	ds_read_b128 v[44:47], v140 offset:39936
	s_add_u32 s28, s28, 0x40100
	s_addc_u32 s29, s29, 0
	s_add_i32 m0, s47, 0x4000
	s_nop 0
	global_load_lds_dwordx4 v134, s[28:29]
	s_nop 0
	s_add_i32 m0, s47, 0x6000
	s_nop 0
	global_load_lds_dwordx4 v136, s[28:29]
	s_waitcnt vmcnt(8) lgkmcnt(0)
	s_barrier
	v_mfma_f32_16x16x128_f8f6f4 v[112:115], v[0:7], v[16:23], v[64:67]
	v_mfma_f32_16x16x128_f8f6f4 v[116:119], v[8:15], v[16:23], v[68:71]
	v_mfma_f32_16x16x128_f8f6f4 v[100:103], v[0:7], v[24:31], v[72:75]
	v_mfma_f32_16x16x128_f8f6f4 v[96:99], v[8:15], v[24:31], v[76:79]
	v_mfma_f32_16x16x128_f8f6f4 v[84:87], v[0:7], v[32:39], v[80:83]
	v_mfma_f32_16x16x128_f8f6f4 v[80:83], v[8:15], v[32:39], v[88:91]
	v_mfma_f32_16x16x128_f8f6f4 v[60:63], v[0:7], v[40:47], v[92:95]
	v_mfma_f32_16x16x128_f8f6f4 v[56:59], v[8:15], v[40:47], v[104:107]
	v_mfma_f32_16x16x128_f8f6f4 v[120:123], v[146:153], v[16:23], v[108:111]
	v_mfma_f32_16x16x128_f8f6f4 v[124:127], v[154:161], v[16:23], v[124:127]
	v_mfma_f32_16x16x128_f8f6f4 v[108:111], v[146:153], v[24:31], v[162:165]
	v_mfma_f32_16x16x128_f8f6f4 v[104:107], v[154:161], v[24:31], v[166:169]
	v_mfma_f32_16x16x128_f8f6f4 v[92:95], v[146:153], v[32:39], v[170:173]
	v_mfma_f32_16x16x128_f8f6f4 v[88:91], v[154:161], v[32:39], v[174:177]
	v_mfma_f32_16x16x128_f8f6f4 v[76:79], v[146:153], v[40:47], v[178:181]
	v_mfma_f32_16x16x128_f8f6f4 v[72:75], v[154:161], v[40:47], v[182:185]
	s_barrier
	ds_read_b128 v[24:27], v140 offset:49152
	ds_read_b128 v[28:31], v140 offset:50176
	ds_read_b128 v[162:165], v140 offset:51200
	ds_read_b128 v[166:169], v140 offset:52224
	ds_read_b128 v[170:173], v140 offset:53248
	ds_read_b128 v[174:177], v140 offset:54272
	ds_read_b128 v[178:181], v140 offset:55296
	ds_read_b128 v[182:185], v140 offset:56320
	s_add_i32 m0, s47, 0x18000
	s_nop 0
	global_load_lds_dwordx4 v135, s[34:35]
	s_nop 0
	s_add_i32 m0, s47, 0x1a000
	s_nop 0
	global_load_lds_dwordx4 v137, s[34:35]
	s_add_u32 s28, s26, 0x40180
	s_addc_u32 s29, s27, 0
	s_add_i32 m0, s47, 0x1c000
	s_nop 0
	global_load_lds_dwordx4 v135, s[28:29]
	s_nop 0
	s_add_i32 m0, s47, 0x1e000
	s_nop 0
	global_load_lds_dwordx4 v137, s[28:29]
	s_nop 0
	s_add_i32 m0, s47, 0x8000
	s_nop 0
	global_load_lds_dwordx4 v134, s[30:31]
	s_nop 0
	s_add_i32 m0, s47, 0xa000
	s_nop 0
	global_load_lds_dwordx4 v136, s[30:31]
	s_waitcnt vmcnt(8) lgkmcnt(0)
	s_barrier
	v_mfma_f32_16x16x128_f8f6f4 v[52:55], v[0:7], v[24:31], v[186:189]
	v_mfma_f32_16x16x128_f8f6f4 v[48:51], v[8:15], v[24:31], v[190:193]
	v_mfma_f32_16x16x128_f8f6f4 v[36:39], v[0:7], v[162:169], v[194:197]
	v_mfma_f32_16x16x128_f8f6f4 v[32:35], v[8:15], v[162:169], v[198:201]
	v_mfma_f32_16x16x128_f8f6f4 v[20:23], v[0:7], v[170:177], v[202:205]
	v_mfma_f32_16x16x128_f8f6f4 v[16:19], v[8:15], v[170:177], v[206:209]
	v_mfma_f32_16x16x128_f8f6f4 v[4:7], v[0:7], v[178:185], v[210:213]
	v_mfma_f32_16x16x128_f8f6f4 v[0:3], v[8:15], v[178:185], v[214:217]
	v_mfma_f32_16x16x128_f8f6f4 v[68:71], v[146:153], v[24:31], v[218:221]
	v_mfma_f32_16x16x128_f8f6f4 v[64:67], v[154:161], v[24:31], v[222:225]
	v_mfma_f32_16x16x128_f8f6f4 v[44:47], v[146:153], v[162:169], v[226:229]
	v_mfma_f32_16x16x128_f8f6f4 v[40:43], v[154:161], v[162:169], v[230:233]
	v_mfma_f32_16x16x128_f8f6f4 v[28:31], v[146:153], v[170:177], v[234:237]
	v_mfma_f32_16x16x128_f8f6f4 v[24:27], v[154:161], v[170:177], v[238:241]
	v_mfma_f32_16x16x128_f8f6f4 v[12:15], v[146:153], v[178:185], v[242:245]
	v_mfma_f32_16x16x128_f8f6f4 v[8:11], v[154:161], v[178:185], v[246:249]
	s_barrier
	s_add_u32 s17, s26, 0x200
	s_addc_u32 s54, s27, 0
	s_mov_b32 s55, 0
	.p2alignl 6, 3212836864

.LBB0_1487:
	ds_read_b128 v[0:3], v153
	ds_read_b128 v[4:7], v153 offset:1024
	ds_read_b128 v[8:11], v153 offset:2048
	ds_read_b128 v[12:15], v153 offset:3072
	ds_read_b128 v[16:19], v154
	ds_read_b128 v[20:23], v154 offset:1024
	ds_read_b128 v[24:27], v154 offset:2048
	ds_read_b128 v[28:31], v154 offset:3072
	ds_read_b128 v[32:35], v155
	ds_read_b128 v[36:39], v155 offset:1024
	ds_read_b128 v[40:43], v155 offset:2048
	ds_read_b128 v[44:47], v155 offset:3072
	ds_read_b128 v[48:51], v155 offset:4096
	ds_read_b128 v[52:55], v155 offset:5120
	ds_read_b128 v[56:59], v155 offset:6144
	ds_read_b128 v[60:63], v155 offset:7168
	s_add_u32 s26, s28, 0x100
	s_addc_u32 s27, s29, 0
	s_add_u32 s36, s24, 0x100
	s_addc_u32 s37, s25, 0
	s_add_u32 s30, s28, 0x180
	s_addc_u32 s31, s29, 0
	s_add_u32 s34, s24, 0x180
	s_addc_u32 s35, s25, 0
	s_add_u32 s52, s28, 0xe0080
	s_addc_u32 s53, s29, 0
	s_add_i32 m0, s44, 0xc000
	s_nop 0
	global_load_lds_dwordx4 v149, s[52:53]
	s_nop 0
	s_add_i32 m0, s44, 0xe000
	s_nop 0
	global_load_lds_dwordx4 v151, s[52:53]
	s_waitcnt vmcnt(8) lgkmcnt(0)
	s_barrier
	v_mfma_f32_16x16x128_f8f6f4 v[64:67], v[0:7], v[32:39], 0
	v_mfma_f32_16x16x128_f8f6f4 v[68:71], v[8:15], v[32:39], 0
	v_mfma_f32_16x16x128_f8f6f4 v[76:79], v[8:15], v[40:47], 0
	v_mfma_f32_16x16x128_f8f6f4 v[72:75], v[0:7], v[40:47], 0
	v_mfma_f32_16x16x128_f8f6f4 v[80:83], v[0:7], v[48:55], 0
	v_mfma_f32_16x16x128_f8f6f4 v[88:91], v[8:15], v[48:55], 0
	v_mfma_f32_16x16x128_f8f6f4 v[104:107], v[8:15], v[56:63], 0
	v_mfma_f32_16x16x128_f8f6f4 v[92:95], v[0:7], v[56:63], 0
	v_mfma_f32_16x16x128_f8f6f4 v[108:111], v[16:23], v[32:39], 0
	v_mfma_f32_16x16x128_f8f6f4 v[124:127], v[24:31], v[32:39], 0
	v_mfma_f32_16x16x128_f8f6f4 v[162:165], v[24:31], v[40:47], 0
	v_mfma_f32_16x16x128_f8f6f4 v[158:161], v[16:23], v[40:47], 0
	v_mfma_f32_16x16x128_f8f6f4 v[166:169], v[16:23], v[48:55], 0
	v_mfma_f32_16x16x128_f8f6f4 v[170:173], v[24:31], v[48:55], 0
	v_mfma_f32_16x16x128_f8f6f4 v[178:181], v[24:31], v[56:63], 0
	v_mfma_f32_16x16x128_f8f6f4 v[174:177], v[16:23], v[56:63], 0
	s_barrier
	ds_read_b128 v[32:35], v155 offset:16384
	ds_read_b128 v[36:39], v155 offset:17408
	ds_read_b128 v[40:43], v155 offset:18432
	ds_read_b128 v[44:47], v155 offset:19456
	ds_read_b128 v[48:51], v155 offset:20480
	ds_read_b128 v[52:55], v155 offset:21504
	ds_read_b128 v[56:59], v155 offset:22528
	ds_read_b128 v[60:63], v155 offset:23552
	s_add_i32 m0, s44, 0x10000
	s_nop 0
	global_load_lds_dwordx4 v150, s[36:37]
	s_nop 0
	s_add_i32 m0, s44, 0x12000
	s_nop 0
	global_load_lds_dwordx4 v152, s[36:37]
	s_add_u32 s36, s24, 0xe0100
	s_addc_u32 s37, s25, 0
	s_add_i32 m0, s44, 0x14000
	s_nop 0
	global_load_lds_dwordx4 v150, s[36:37]
	s_nop 0
	s_add_i32 m0, s44, 0x16000
	s_nop 0
	global_load_lds_dwordx4 v152, s[36:37]
	s_nop 0
	s_add_i32 m0, s44, 0
	s_nop 0
	global_load_lds_dwordx4 v149, s[26:27]
	s_nop 0
	s_add_i32 m0, s44, 0x2000
	s_nop 0
	global_load_lds_dwordx4 v151, s[26:27]
	s_waitcnt vmcnt(8) lgkmcnt(0)
	s_barrier
	v_mfma_f32_16x16x128_f8f6f4 v[190:193], v[0:7], v[32:39], 0
	v_mfma_f32_16x16x128_f8f6f4 v[194:197], v[8:15], v[32:39], 0
	v_mfma_f32_16x16x128_f8f6f4 v[202:205], v[8:15], v[40:47], 0
	v_mfma_f32_16x16x128_f8f6f4 v[198:201], v[0:7], v[40:47], 0
	v_mfma_f32_16x16x128_f8f6f4 v[206:209], v[0:7], v[48:55], 0
	v_mfma_f32_16x16x128_f8f6f4 v[210:213], v[8:15], v[48:55], 0
	v_mfma_f32_16x16x128_f8f6f4 v[218:221], v[8:15], v[56:63], 0
	v_mfma_f32_16x16x128_f8f6f4 v[214:217], v[0:7], v[56:63], 0
	v_mfma_f32_16x16x128_f8f6f4 v[222:225], v[16:23], v[32:39], 0
	v_mfma_f32_16x16x128_f8f6f4 v[226:229], v[24:31], v[32:39], 0
	v_mfma_f32_16x16x128_f8f6f4 v[234:237], v[24:31], v[40:47], 0
	v_mfma_f32_16x16x128_f8f6f4 v[230:233], v[16:23], v[40:47], 0
	v_mfma_f32_16x16x128_f8f6f4 v[238:241], v[16:23], v[48:55], 0
	v_mfma_f32_16x16x128_f8f6f4 v[242:245], v[24:31], v[48:55], 0
	v_mfma_f32_16x16x128_f8f6f4 v[250:253], v[24:31], v[56:63], 0
	v_mfma_f32_16x16x128_f8f6f4 v[246:249], v[16:23], v[56:63], 0
	s_barrier
	ds_read_b128 v[0:3], v156
	ds_read_b128 v[4:7], v156 offset:1024
	ds_read_b128 v[16:19], v156 offset:2048
	ds_read_b128 v[20:23], v156 offset:3072
	ds_read_b128 v[132:135], v157
	ds_read_b128 v[136:139], v157 offset:1024
	ds_read_b128 v[140:143], v157 offset:2048
	ds_read_b128 v[144:147], v157 offset:3072
	ds_read_b128 v[8:11], v155 offset:32768
	ds_read_b128 v[12:15], v155 offset:33792
	ds_read_b128 v[24:27], v155 offset:34816
	ds_read_b128 v[28:31], v155 offset:35840
	ds_read_b128 v[32:35], v155 offset:36864
	ds_read_b128 v[36:39], v155 offset:37888
	ds_read_b128 v[40:43], v155 offset:38912
	ds_read_b128 v[44:47], v155 offset:39936
	s_add_u32 s28, s28, 0xe0100
	s_addc_u32 s29, s29, 0
	s_add_i32 m0, s44, 0x4000
	s_nop 0
	global_load_lds_dwordx4 v149, s[28:29]
	s_nop 0
	s_add_i32 m0, s44, 0x6000
	s_nop 0
	global_load_lds_dwordx4 v151, s[28:29]
	s_waitcnt vmcnt(8) lgkmcnt(0)
	s_barrier
	v_mfma_f32_16x16x128_f8f6f4 v[112:115], v[0:7], v[8:15], v[64:67]
	v_mfma_f32_16x16x128_f8f6f4 v[116:119], v[16:23], v[8:15], v[68:71]
	v_mfma_f32_16x16x128_f8f6f4 v[100:103], v[0:7], v[24:31], v[72:75]
	v_mfma_f32_16x16x128_f8f6f4 v[96:99], v[16:23], v[24:31], v[76:79]
	v_mfma_f32_16x16x128_f8f6f4 v[84:87], v[0:7], v[32:39], v[80:83]
	v_mfma_f32_16x16x128_f8f6f4 v[80:83], v[16:23], v[32:39], v[88:91]
	v_mfma_f32_16x16x128_f8f6f4 v[60:63], v[0:7], v[40:47], v[92:95]
	v_mfma_f32_16x16x128_f8f6f4 v[52:55], v[16:23], v[40:47], v[104:107]
	v_mfma_f32_16x16x128_f8f6f4 v[120:123], v[132:139], v[8:15], v[108:111]
	v_mfma_f32_16x16x128_f8f6f4 v[124:127], v[140:147], v[8:15], v[124:127]
	v_mfma_f32_16x16x128_f8f6f4 v[108:111], v[132:139], v[24:31], v[158:161]
	v_mfma_f32_16x16x128_f8f6f4 v[104:107], v[140:147], v[24:31], v[162:165]
	v_mfma_f32_16x16x128_f8f6f4 v[92:95], v[132:139], v[32:39], v[166:169]
	v_mfma_f32_16x16x128_f8f6f4 v[88:91], v[140:147], v[32:39], v[170:173]
	v_mfma_f32_16x16x128_f8f6f4 v[56:59], v[132:139], v[40:47], v[174:177]
	v_mfma_f32_16x16x128_f8f6f4 v[48:51], v[140:147], v[40:47], v[178:181]
	s_barrier
	ds_read_b128 v[158:161], v155 offset:49152
	ds_read_b128 v[162:165], v155 offset:50176
	ds_read_b128 v[166:169], v155 offset:51200
	ds_read_b128 v[170:173], v155 offset:52224
	ds_read_b128 v[174:177], v155 offset:53248
	ds_read_b128 v[178:181], v155 offset:54272
	ds_read_b128 v[182:185], v155 offset:55296
	ds_read_b128 v[186:189], v155 offset:56320
	s_add_i32 m0, s44, 0x18000
	s_nop 0
	global_load_lds_dwordx4 v150, s[34:35]
	s_nop 0
	s_add_i32 m0, s44, 0x1a000
	s_nop 0
	global_load_lds_dwordx4 v152, s[34:35]
	s_add_u32 s28, s24, 0xe0180
	s_addc_u32 s29, s25, 0
	s_add_i32 m0, s44, 0x1c000
	s_nop 0
	global_load_lds_dwordx4 v150, s[28:29]
	s_nop 0
	s_add_i32 m0, s44, 0x1e000
	s_nop 0
	global_load_lds_dwordx4 v152, s[28:29]
	s_nop 0
	s_add_i32 m0, s44, 0x8000
	s_nop 0
	global_load_lds_dwordx4 v149, s[30:31]
	s_nop 0
	s_add_i32 m0, s44, 0xa000
	s_nop 0
	global_load_lds_dwordx4 v151, s[30:31]
	s_waitcnt vmcnt(8) lgkmcnt(0)
	s_barrier
	v_mfma_f32_16x16x128_f8f6f4 v[68:71], v[0:7], v[158:165], v[190:193]
	v_mfma_f32_16x16x128_f8f6f4 v[64:67], v[16:23], v[158:165], v[194:197]
	v_mfma_f32_16x16x128_f8f6f4 v[36:39], v[16:23], v[166:173], v[202:205]
	v_mfma_f32_16x16x128_f8f6f4 v[44:47], v[0:7], v[166:173], v[198:201]
	v_mfma_f32_16x16x128_f8f6f4 v[28:31], v[0:7], v[174:181], v[206:209]
	v_mfma_f32_16x16x128_f8f6f4 v[24:27], v[16:23], v[174:181], v[210:213]
	v_mfma_f32_16x16x128_f8f6f4 v[8:11], v[16:23], v[182:189], v[218:221]
	v_mfma_f32_16x16x128_f8f6f4 v[12:15], v[0:7], v[182:189], v[214:217]
	v_mfma_f32_16x16x128_f8f6f4 v[76:79], v[132:139], v[158:165], v[222:225]
	v_mfma_f32_16x16x128_f8f6f4 v[72:75], v[140:147], v[158:165], v[226:229]
	v_mfma_f32_16x16x128_f8f6f4 v[32:35], v[140:147], v[166:173], v[234:237]
	v_mfma_f32_16x16x128_f8f6f4 v[40:43], v[132:139], v[166:173], v[230:233]
	v_mfma_f32_16x16x128_f8f6f4 v[20:23], v[132:139], v[174:181], v[238:241]
	v_mfma_f32_16x16x128_f8f6f4 v[16:19], v[140:147], v[174:181], v[242:245]
	v_mfma_f32_16x16x128_f8f6f4 v[0:3], v[140:147], v[182:189], v[250:253]
	v_mfma_f32_16x16x128_f8f6f4 v[4:7], v[132:139], v[182:189], v[246:249]
	s_barrier
	s_add_u32 s23, s24, 0x200
	s_addc_u32 s51, s25, 0
	s_mov_b32 s52, 0
	.p2alignl 6, 3212836864
